# v038 + the 80 redundant s_waitcnt lgkmcnt(0) directly after K-loop barriers (ahead of each MFMA block) removed
# speedup vs baseline: 1.0125x; 1.0125x over previous
.LBB0_260:
	s_ashr_i32 s69, s68, 31
	s_lshl_b64 s[26:27], s[68:69], 20
	v_readlane_b32 s8, v254, 56
	v_readlane_b32 s9, v254, 57
	s_add_u32 s70, s8, s26
	s_addc_u32 s71, s9, s27
	s_and_b64 s[26:27], s[0:1], exec
	s_cselect_b32 s69, s71, s83
	s_cselect_b32 s75, s70, s82
	s_ashr_i32 s57, s56, 31
	s_lshl_b64 s[26:27], s[56:57], 20
	s_add_u32 s72, s84, s26
	s_addc_u32 s73, s85, s27
	s_and_b64 s[26:27], s[0:1], exec
	s_cselect_b32 s57, s73, s81
	s_cselect_b32 s96, s72, s80
	s_add_u32 s97, s80, 0x10000
	s_addc_u32 vcc_lo, s81, 0
	s_add_u32 s80, s82, 0x80080
	s_addc_u32 s81, s83, 0
	s_mov_b32 vcc_hi, -2
	ds_read_b128 v[144:147], v170
	ds_read_b128 v[148:151], v170 offset:1024
	ds_read_b128 v[174:177], v170 offset:2048
	ds_read_b128 v[178:181], v170 offset:3072
	ds_read_b128 v[182:185], v171
	ds_read_b128 v[186:189], v171 offset:1024
	ds_read_b128 v[190:193], v171 offset:2048
	ds_read_b128 v[194:197], v171 offset:3072
	s_add_u32 s26, s80, 0xfff80080
	s_addc_u32 s27, s81, -1
	s_cmp_eq_u32 vcc_hi, 28
	s_cselect_b32 s83, s69, s27
	s_cselect_b32 s82, s75, s26
	s_cselect_b32 s27, s57, vcc_lo
	s_cselect_b32 s26, s96, s97
	v_lshl_add_u64 v[152:153], s[80:81], 0, v[134:135]
	s_add_i32 m0, s87, 0xc000
	ds_read_b128 v[198:201], v172
	ds_read_b128 v[202:205], v172 offset:1024
	ds_read_b128 v[206:209], v172 offset:2048
	ds_read_b128 v[210:213], v172 offset:3072
	ds_read_b128 v[214:217], v172 offset:4096
	ds_read_b128 v[220:223], v172 offset:5120
	ds_read_b128 v[224:227], v172 offset:6144
	ds_read_b128 v[228:231], v172 offset:7168
	global_load_lds_dwordx4 v[152:153], off
	v_lshl_add_u64 v[152:153], s[80:81], 0, v[138:139]
	s_add_i32 m0, s87, 0xe000
	s_nop 0
	global_load_lds_dwordx4 v[152:153], off
	s_waitcnt vmcnt(8)
	s_waitcnt lgkmcnt(0)
	s_barrier
	v_mfma_f32_16x16x32_bf16 v[122:125], v[144:147], v[198:201], 0
	v_mfma_f32_16x16x32_bf16 v[118:121], v[174:177], v[198:201], 0
	v_mfma_f32_16x16x32_bf16 v[106:109], v[144:147], v[206:209], 0
	v_mfma_f32_16x16x32_bf16 v[102:105], v[174:177], v[206:209], 0
	v_mfma_f32_16x16x32_bf16 v[90:93], v[144:147], v[214:217], 0
	v_mfma_f32_16x16x32_bf16 v[86:89], v[174:177], v[214:217], 0
	v_mfma_f32_16x16x32_bf16 v[74:77], v[144:147], v[224:227], 0
	v_mfma_f32_16x16x32_bf16 v[70:73], v[174:177], v[224:227], 0
	v_mfma_f32_16x16x32_bf16 v[122:125], v[148:151], v[202:205], v[122:125]
	v_mfma_f32_16x16x32_bf16 v[118:121], v[178:181], v[202:205], v[118:121]
	v_mfma_f32_16x16x32_bf16 v[106:109], v[148:151], v[210:213], v[106:109]
	v_mfma_f32_16x16x32_bf16 v[102:105], v[178:181], v[210:213], v[102:105]
	v_mfma_f32_16x16x32_bf16 v[90:93], v[148:151], v[220:223], v[90:93]
	v_mfma_f32_16x16x32_bf16 v[86:89], v[178:181], v[220:223], v[86:89]
	v_mfma_f32_16x16x32_bf16 v[74:77], v[148:151], v[228:231], v[74:77]
	v_mfma_f32_16x16x32_bf16 v[70:73], v[178:181], v[228:231], v[70:73]
	v_mfma_f32_16x16x32_bf16 v[126:129], v[182:185], v[198:201], 0
	v_mfma_f32_16x16x32_bf16 v[114:117], v[190:193], v[198:201], 0
	v_mfma_f32_16x16x32_bf16 v[110:113], v[182:185], v[206:209], 0
	v_mfma_f32_16x16x32_bf16 v[98:101], v[190:193], v[206:209], 0
	v_mfma_f32_16x16x32_bf16 v[94:97], v[182:185], v[214:217], 0
	v_mfma_f32_16x16x32_bf16 v[82:85], v[190:193], v[214:217], 0
	v_mfma_f32_16x16x32_bf16 v[78:81], v[182:185], v[224:227], 0
	v_mfma_f32_16x16x32_bf16 v[66:69], v[190:193], v[224:227], 0
	v_mfma_f32_16x16x32_bf16 v[126:129], v[186:189], v[202:205], v[126:129]
	v_mfma_f32_16x16x32_bf16 v[114:117], v[194:197], v[202:205], v[114:117]
	v_mfma_f32_16x16x32_bf16 v[110:113], v[186:189], v[210:213], v[110:113]
	v_mfma_f32_16x16x32_bf16 v[98:101], v[194:197], v[210:213], v[98:101]
	v_mfma_f32_16x16x32_bf16 v[94:97], v[186:189], v[220:223], v[94:97]
	v_mfma_f32_16x16x32_bf16 v[82:85], v[194:197], v[220:223], v[82:85]
	v_mfma_f32_16x16x32_bf16 v[78:81], v[186:189], v[228:231], v[78:81]
	v_mfma_f32_16x16x32_bf16 v[66:69], v[194:197], v[228:231], v[66:69]
	s_barrier
	v_lshl_add_u64 v[152:153], s[26:27], 0, v[162:163]
	s_add_i32 s26, s94, s86
	s_mov_b32 m0, s26
	ds_read_b128 v[198:201], v172 offset:16384
	ds_read_b128 v[202:205], v172 offset:17408
	ds_read_b128 v[206:209], v172 offset:18432
	ds_read_b128 v[210:213], v172 offset:19456
	ds_read_b128 v[214:217], v172 offset:20480
	ds_read_b128 v[220:223], v172 offset:21504
	ds_read_b128 v[224:227], v172 offset:22528
	ds_read_b128 v[228:231], v172 offset:23552
	global_load_lds_dwordx4 v[152:153], off
	v_lshl_add_u64 v[232:233], v[152:153], 0, s[10:11]
	s_add_i32 m0, s26, 0x2000
	s_add_i32 s26, s95, s86
	global_load_lds_dwordx4 v[232:233], off
	v_lshl_add_u64 v[232:233], v[152:153], 0, s[12:13]
	s_mov_b32 m0, s26
	v_lshl_add_u64 v[234:235], s[82:83], 0, v[132:133]
	global_load_lds_dwordx4 v[232:233], off
	v_lshl_add_u64 v[232:233], v[152:153], 0, s[14:15]
	s_add_i32 m0, s26, 0x2000
	s_nop 0
	global_load_lds_dwordx4 v[232:233], off
	v_lshl_add_u64 v[232:233], s[82:83], 0, v[130:131]
	s_mov_b32 m0, s87
	s_nop 0
	global_load_lds_dwordx4 v[232:233], off
	s_mov_b32 m0, s88
	s_nop 0
	global_load_lds_dwordx4 v[234:235], off
	s_waitcnt vmcnt(8)
	s_waitcnt lgkmcnt(0)
	s_barrier
	v_mfma_f32_16x16x32_bf16 v[58:61], v[144:147], v[198:201], 0
	v_mfma_f32_16x16x32_bf16 v[54:57], v[174:177], v[198:201], 0
	v_mfma_f32_16x16x32_bf16 v[42:45], v[144:147], v[206:209], 0
	v_mfma_f32_16x16x32_bf16 v[38:41], v[174:177], v[206:209], 0
	v_mfma_f32_16x16x32_bf16 v[26:29], v[144:147], v[214:217], 0
	v_mfma_f32_16x16x32_bf16 v[22:25], v[174:177], v[214:217], 0
	v_mfma_f32_16x16x32_bf16 v[10:13], v[144:147], v[224:227], 0
	v_mfma_f32_16x16x32_bf16 v[6:9], v[174:177], v[224:227], 0
	v_mfma_f32_16x16x32_bf16 v[58:61], v[148:151], v[202:205], v[58:61]
	v_mfma_f32_16x16x32_bf16 v[54:57], v[178:181], v[202:205], v[54:57]
	v_mfma_f32_16x16x32_bf16 v[42:45], v[148:151], v[210:213], v[42:45]
	v_mfma_f32_16x16x32_bf16 v[38:41], v[178:181], v[210:213], v[38:41]
	v_mfma_f32_16x16x32_bf16 v[26:29], v[148:151], v[220:223], v[26:29]
	v_mfma_f32_16x16x32_bf16 v[22:25], v[178:181], v[220:223], v[22:25]
	v_mfma_f32_16x16x32_bf16 v[10:13], v[148:151], v[228:231], v[10:13]
	v_mfma_f32_16x16x32_bf16 v[6:9], v[178:181], v[228:231], v[6:9]
	v_mfma_f32_16x16x32_bf16 v[62:65], v[182:185], v[198:201], 0
	v_mfma_f32_16x16x32_bf16 v[50:53], v[190:193], v[198:201], 0
	v_mfma_f32_16x16x32_bf16 v[46:49], v[182:185], v[206:209], 0
	v_mfma_f32_16x16x32_bf16 v[34:37], v[190:193], v[206:209], 0
	v_mfma_f32_16x16x32_bf16 v[30:33], v[182:185], v[214:217], 0
	v_mfma_f32_16x16x32_bf16 v[18:21], v[190:193], v[214:217], 0
	v_mfma_f32_16x16x32_bf16 v[14:17], v[182:185], v[224:227], 0
	v_mfma_f32_16x16x32_bf16 v[2:5], v[190:193], v[224:227], 0
	v_mfma_f32_16x16x32_bf16 v[62:65], v[186:189], v[202:205], v[62:65]
	v_mfma_f32_16x16x32_bf16 v[50:53], v[194:197], v[202:205], v[50:53]
	v_mfma_f32_16x16x32_bf16 v[46:49], v[186:189], v[210:213], v[46:49]
	v_mfma_f32_16x16x32_bf16 v[34:37], v[194:197], v[210:213], v[34:37]
	v_mfma_f32_16x16x32_bf16 v[30:33], v[186:189], v[220:223], v[30:33]
	v_mfma_f32_16x16x32_bf16 v[18:21], v[194:197], v[220:223], v[18:21]
	v_mfma_f32_16x16x32_bf16 v[14:17], v[186:189], v[228:231], v[14:17]
	v_mfma_f32_16x16x32_bf16 v[2:5], v[194:197], v[228:231], v[2:5]
	s_barrier
	s_add_i32 s33, 0, 0x18000
	v_add_u32_e32 v136, s33, v167
	s_add_i32 s8, 0, 0x1c000
	ds_read_b128 v[144:147], v136
	ds_read_b128 v[148:151], v136 offset:1024
	ds_read_b128 v[174:177], v136 offset:2048
	ds_read_b128 v[178:181], v136 offset:3072
	v_add_u32_e32 v136, s8, v167
	ds_read_b128 v[182:185], v136
	ds_read_b128 v[186:189], v136 offset:1024
	ds_read_b128 v[190:193], v136 offset:2048
	ds_read_b128 v[194:197], v136 offset:3072
	s_add_u32 s26, s82, 0x80000
	s_addc_u32 s27, s83, 0
	s_mov_b32 m0, s89
	v_lshl_add_u64 v[236:237], s[26:27], 0, v[130:131]
	ds_read_b128 v[198:201], v172 offset:32768
	ds_read_b128 v[202:205], v172 offset:33792
	ds_read_b128 v[206:209], v172 offset:34816
	ds_read_b128 v[210:213], v172 offset:35840
	ds_read_b128 v[214:217], v172 offset:36864
	ds_read_b128 v[220:223], v172 offset:37888
	ds_read_b128 v[224:227], v172 offset:38912
	ds_read_b128 v[228:231], v172 offset:39936
	global_load_lds_dwordx4 v[236:237], off
	v_lshl_add_u64 v[236:237], s[26:27], 0, v[132:133]
	s_mov_b32 m0, s90
	s_nop 0
	global_load_lds_dwordx4 v[236:237], off
	s_waitcnt vmcnt(8)
	s_waitcnt lgkmcnt(0)
	s_barrier
	v_mfma_f32_16x16x32_bf16 v[122:125], v[144:147], v[198:201], v[122:125]
	v_mfma_f32_16x16x32_bf16 v[118:121], v[174:177], v[198:201], v[118:121]
	v_mfma_f32_16x16x32_bf16 v[106:109], v[144:147], v[206:209], v[106:109]
	v_mfma_f32_16x16x32_bf16 v[102:105], v[174:177], v[206:209], v[102:105]
	v_mfma_f32_16x16x32_bf16 v[90:93], v[144:147], v[214:217], v[90:93]
	v_mfma_f32_16x16x32_bf16 v[86:89], v[174:177], v[214:217], v[86:89]
	v_mfma_f32_16x16x32_bf16 v[74:77], v[144:147], v[224:227], v[74:77]
	v_mfma_f32_16x16x32_bf16 v[70:73], v[174:177], v[224:227], v[70:73]
	v_mfma_f32_16x16x32_bf16 v[122:125], v[148:151], v[202:205], v[122:125]
	v_mfma_f32_16x16x32_bf16 v[118:121], v[178:181], v[202:205], v[118:121]
	v_mfma_f32_16x16x32_bf16 v[106:109], v[148:151], v[210:213], v[106:109]
	v_mfma_f32_16x16x32_bf16 v[102:105], v[178:181], v[210:213], v[102:105]
	v_mfma_f32_16x16x32_bf16 v[90:93], v[148:151], v[220:223], v[90:93]
	v_mfma_f32_16x16x32_bf16 v[86:89], v[178:181], v[220:223], v[86:89]
	v_mfma_f32_16x16x32_bf16 v[74:77], v[148:151], v[228:231], v[74:77]
	v_mfma_f32_16x16x32_bf16 v[70:73], v[178:181], v[228:231], v[70:73]
	v_mfma_f32_16x16x32_bf16 v[126:129], v[182:185], v[198:201], v[126:129]
	v_mfma_f32_16x16x32_bf16 v[114:117], v[190:193], v[198:201], v[114:117]
	v_mfma_f32_16x16x32_bf16 v[110:113], v[182:185], v[206:209], v[110:113]
	v_mfma_f32_16x16x32_bf16 v[98:101], v[190:193], v[206:209], v[98:101]
	v_mfma_f32_16x16x32_bf16 v[94:97], v[182:185], v[214:217], v[94:97]
	v_mfma_f32_16x16x32_bf16 v[82:85], v[190:193], v[214:217], v[82:85]
	v_mfma_f32_16x16x32_bf16 v[78:81], v[182:185], v[224:227], v[78:81]
	v_mfma_f32_16x16x32_bf16 v[66:69], v[190:193], v[224:227], v[66:69]
	v_mfma_f32_16x16x32_bf16 v[126:129], v[186:189], v[202:205], v[126:129]
	v_mfma_f32_16x16x32_bf16 v[114:117], v[194:197], v[202:205], v[114:117]
	v_mfma_f32_16x16x32_bf16 v[110:113], v[186:189], v[210:213], v[110:113]
	v_mfma_f32_16x16x32_bf16 v[98:101], v[194:197], v[210:213], v[98:101]
	v_mfma_f32_16x16x32_bf16 v[94:97], v[186:189], v[220:223], v[94:97]
	v_mfma_f32_16x16x32_bf16 v[82:85], v[194:197], v[220:223], v[82:85]
	v_mfma_f32_16x16x32_bf16 v[78:81], v[186:189], v[228:231], v[78:81]
	v_mfma_f32_16x16x32_bf16 v[66:69], v[194:197], v[228:231], v[66:69]
	s_barrier
	s_add_i32 s9, s33, s86
	v_lshl_add_u64 v[236:237], v[152:153], 0, s[20:21]
	s_mov_b32 m0, s9
	ds_read_b128 v[198:201], v172 offset:49152
	ds_read_b128 v[202:205], v172 offset:50176
	ds_read_b128 v[206:209], v172 offset:51200
	ds_read_b128 v[210:213], v172 offset:52224
	ds_read_b128 v[214:217], v172 offset:53248
	ds_read_b128 v[220:223], v172 offset:54272
	ds_read_b128 v[224:227], v172 offset:55296
	ds_read_b128 v[228:231], v172 offset:56320
	global_load_lds_dwordx4 v[236:237], off
	v_lshl_add_u64 v[236:237], v[152:153], 0, s[22:23]
	s_add_i32 m0, s9, 0x2000
	s_add_i32 s8, s8, s86
	global_load_lds_dwordx4 v[236:237], off
	v_lshl_add_u64 v[236:237], v[152:153], 0, s[40:41]
	s_mov_b32 m0, s8
	v_lshl_add_u64 v[152:153], v[152:153], 0, s[44:45]
	global_load_lds_dwordx4 v[236:237], off
	s_add_i32 m0, s8, 0x2000
	s_nop 0
	global_load_lds_dwordx4 v[152:153], off
	v_lshl_add_u64 v[152:153], v[232:233], 0, s[24:25]
	s_mov_b32 m0, s91
	s_nop 0
	global_load_lds_dwordx4 v[152:153], off
	v_lshl_add_u64 v[152:153], v[234:235], 0, s[24:25]
	s_mov_b32 m0, s92
	s_nop 0
	global_load_lds_dwordx4 v[152:153], off
	s_waitcnt vmcnt(8)
	s_waitcnt lgkmcnt(0)
	s_barrier
	v_mfma_f32_16x16x32_bf16 v[58:61], v[144:147], v[198:201], v[58:61]
	v_mfma_f32_16x16x32_bf16 v[54:57], v[174:177], v[198:201], v[54:57]
	v_mfma_f32_16x16x32_bf16 v[42:45], v[144:147], v[206:209], v[42:45]
	v_mfma_f32_16x16x32_bf16 v[38:41], v[174:177], v[206:209], v[38:41]
	v_mfma_f32_16x16x32_bf16 v[26:29], v[144:147], v[214:217], v[26:29]
	v_mfma_f32_16x16x32_bf16 v[22:25], v[174:177], v[214:217], v[22:25]
	v_mfma_f32_16x16x32_bf16 v[10:13], v[144:147], v[224:227], v[10:13]
	v_mfma_f32_16x16x32_bf16 v[6:9], v[174:177], v[224:227], v[6:9]
	v_mfma_f32_16x16x32_bf16 v[58:61], v[148:151], v[202:205], v[58:61]
	v_mfma_f32_16x16x32_bf16 v[54:57], v[178:181], v[202:205], v[54:57]
	v_mfma_f32_16x16x32_bf16 v[42:45], v[148:151], v[210:213], v[42:45]
	v_mfma_f32_16x16x32_bf16 v[38:41], v[178:181], v[210:213], v[38:41]
	v_mfma_f32_16x16x32_bf16 v[26:29], v[148:151], v[220:223], v[26:29]
	v_mfma_f32_16x16x32_bf16 v[22:25], v[178:181], v[220:223], v[22:25]
	v_mfma_f32_16x16x32_bf16 v[10:13], v[148:151], v[228:231], v[10:13]
	v_mfma_f32_16x16x32_bf16 v[6:9], v[178:181], v[228:231], v[6:9]
	v_mfma_f32_16x16x32_bf16 v[62:65], v[182:185], v[198:201], v[62:65]
	v_mfma_f32_16x16x32_bf16 v[50:53], v[190:193], v[198:201], v[50:53]
	v_mfma_f32_16x16x32_bf16 v[46:49], v[182:185], v[206:209], v[46:49]
	v_mfma_f32_16x16x32_bf16 v[34:37], v[190:193], v[206:209], v[34:37]
	v_mfma_f32_16x16x32_bf16 v[30:33], v[182:185], v[214:217], v[30:33]
	v_mfma_f32_16x16x32_bf16 v[18:21], v[190:193], v[214:217], v[18:21]
	v_mfma_f32_16x16x32_bf16 v[14:17], v[182:185], v[224:227], v[14:17]
	v_mfma_f32_16x16x32_bf16 v[2:5], v[190:193], v[224:227], v[2:5]
	v_mfma_f32_16x16x32_bf16 v[62:65], v[186:189], v[202:205], v[62:65]
	v_mfma_f32_16x16x32_bf16 v[50:53], v[194:197], v[202:205], v[50:53]
	v_mfma_f32_16x16x32_bf16 v[46:49], v[186:189], v[210:213], v[46:49]
	v_mfma_f32_16x16x32_bf16 v[34:37], v[194:197], v[210:213], v[34:37]
	v_mfma_f32_16x16x32_bf16 v[30:33], v[186:189], v[220:223], v[30:33]
	v_mfma_f32_16x16x32_bf16 v[18:21], v[194:197], v[220:223], v[18:21]
	v_mfma_f32_16x16x32_bf16 v[14:17], v[186:189], v[228:231], v[14:17]
	v_mfma_f32_16x16x32_bf16 v[2:5], v[194:197], v[228:231], v[2:5]
	s_barrier
	s_add_i32 vcc_hi, vcc_hi, 2
	s_add_u32 s97, s97, 0x10000
	s_addc_u32 vcc_lo, vcc_lo, 0
	s_add_u32 s80, s80, 0x100
	s_addc_u32 s81, s81, 0
	s_cmp_gt_u32 vcc_hi, 29

.LBB0_284:
	s_ashr_i32 s51, s50, 31
	s_lshl_b64 s[26:27], s[50:51], 19
	v_readlane_b32 s54, v254, 58
	v_readlane_b32 s55, v254, 59
	s_add_u32 s54, s54, s26
	s_addc_u32 s55, s55, s27
	s_and_b64 s[26:27], s[0:1], exec
	s_cselect_b32 s51, s55, s73
	s_cselect_b32 s90, s54, s72
	s_ashr_i32 s45, s44, 31
	s_lshl_b64 s[26:27], s[44:45], 19
	s_add_u32 s56, s81, s26
	s_addc_u32 s57, s82, s27
	s_and_b64 s[26:27], s[0:1], exec
	s_cselect_b32 s45, s57, s71
	s_cselect_b32 s91, s56, s70
	s_add_u32 s92, s70, 0x10000
	s_addc_u32 s93, s71, 0
	s_add_u32 s70, s72, 0x40080
	s_addc_u32 s71, s73, 0
	s_mov_b32 s94, -2
	ds_read_b128 v[26:29], v1
	ds_read_b128 v[30:33], v1 offset:1024
	ds_read_b128 v[18:21], v1 offset:2048
	ds_read_b128 v[22:25], v1 offset:3072
	ds_read_b128 v[10:13], v185
	ds_read_b128 v[14:17], v185 offset:1024
	ds_read_b128 v[2:5], v185 offset:2048
	ds_read_b128 v[6:9], v185 offset:3072
	s_add_u32 s26, s70, 0xfffc0080
	s_addc_u32 s27, s71, -1
	s_cmp_eq_u32 s94, 12
	s_cselect_b32 s73, s51, s27
	s_cselect_b32 s72, s90, s26
	s_cselect_b32 s75, s45, s93
	s_cselect_b32 s74, s91, s92
	v_lshl_add_u64 v[176:177], s[70:71], 0, v[168:169]
	s_add_i32 m0, s33, 0xc000
	ds_read_b128 v[190:193], v186
	ds_read_b128 v[194:197], v186 offset:1024
	ds_read_b128 v[198:201], v186 offset:2048
	ds_read_b128 v[202:205], v186 offset:3072
	ds_read_b128 v[206:209], v186 offset:4096
	ds_read_b128 v[210:213], v186 offset:5120
	ds_read_b128 v[220:223], v186 offset:6144
	ds_read_b128 v[224:227], v186 offset:7168
	global_load_lds_dwordx4 v[176:177], off
	v_lshl_add_u64 v[176:177], s[70:71], 0, v[170:171]
	s_add_i32 m0, s33, 0xe000
	s_nop 0
	global_load_lds_dwordx4 v[176:177], off
	s_waitcnt vmcnt(24)
	s_waitcnt lgkmcnt(0)
	s_barrier
	v_mfma_scale_f32_16x16x128_f8f6f4 v[158:161], v[26:33], v[190:197], 0, v187, v188 op_sel_hi:[0,0,0]
	v_mfma_scale_f32_16x16x128_f8f6f4 v[154:157], v[18:25], v[190:197], 0, v187, v188 op_sel_hi:[0,0,0]
	v_mfma_scale_f32_16x16x128_f8f6f4 v[150:153], v[26:33], v[198:205], 0, v187, v188 op_sel_hi:[0,0,0]
	v_mfma_scale_f32_16x16x128_f8f6f4 v[142:145], v[18:25], v[198:205], 0, v187, v188 op_sel_hi:[0,0,0]
	v_mfma_scale_f32_16x16x128_f8f6f4 v[134:137], v[26:33], v[206:213], 0, v187, v188 op_sel_hi:[0,0,0]
	v_mfma_scale_f32_16x16x128_f8f6f4 v[126:129], v[18:25], v[206:213], 0, v187, v188 op_sel_hi:[0,0,0]
	v_mfma_scale_f32_16x16x128_f8f6f4 v[118:121], v[26:33], v[220:227], 0, v187, v188 op_sel_hi:[0,0,0]
	v_mfma_scale_f32_16x16x128_f8f6f4 v[110:113], v[18:25], v[220:227], 0, v187, v188 op_sel_hi:[0,0,0]
	v_mfma_scale_f32_16x16x128_f8f6f4 v[146:149], v[10:17], v[190:197], 0, v187, v188 op_sel_hi:[0,0,0]
	v_mfma_scale_f32_16x16x128_f8f6f4 v[138:141], v[2:9], v[190:197], 0, v187, v188 op_sel_hi:[0,0,0]
	v_mfma_scale_f32_16x16x128_f8f6f4 v[130:133], v[10:17], v[198:205], 0, v187, v188 op_sel_hi:[0,0,0]
	v_mfma_scale_f32_16x16x128_f8f6f4 v[122:125], v[2:9], v[198:205], 0, v187, v188 op_sel_hi:[0,0,0]
	v_mfma_scale_f32_16x16x128_f8f6f4 v[114:117], v[10:17], v[206:213], 0, v187, v188 op_sel_hi:[0,0,0]
	v_mfma_scale_f32_16x16x128_f8f6f4 v[106:109], v[2:9], v[206:213], 0, v187, v188 op_sel_hi:[0,0,0]
	v_mfma_scale_f32_16x16x128_f8f6f4 v[102:105], v[10:17], v[220:227], 0, v187, v188 op_sel_hi:[0,0,0]
	v_mfma_scale_f32_16x16x128_f8f6f4 v[98:101], v[2:9], v[220:227], 0, v187, v188 op_sel_hi:[0,0,0]
	s_barrier
	s_add_i32 s26, s88, s80
	v_lshl_add_u64 v[176:177], s[74:75], 0, v[162:163]
	s_mov_b32 m0, s26
	ds_read_b128 v[190:193], v186 offset:16384
	ds_read_b128 v[194:197], v186 offset:17408
	ds_read_b128 v[198:201], v186 offset:18432
	ds_read_b128 v[202:205], v186 offset:19456
	ds_read_b128 v[206:209], v186 offset:20480
	ds_read_b128 v[210:213], v186 offset:21504
	ds_read_b128 v[220:223], v186 offset:22528
	ds_read_b128 v[224:227], v186 offset:23552
	global_load_lds_dwordx4 v[176:177], off
	v_lshl_add_u64 v[178:179], v[176:177], 0, s[8:9]
	s_add_i32 m0, s26, 0x2000
	s_add_i32 s26, s89, s80
	global_load_lds_dwordx4 v[178:179], off
	v_lshl_add_u64 v[178:179], v[176:177], 0, s[10:11]
	s_mov_b32 m0, s26
	v_lshl_add_u64 v[180:181], s[72:73], 0, v[166:167]
	global_load_lds_dwordx4 v[178:179], off
	v_lshl_add_u64 v[178:179], v[176:177], 0, s[12:13]
	s_add_i32 m0, s26, 0x2000
	s_nop 0
	global_load_lds_dwordx4 v[178:179], off
	v_lshl_add_u64 v[178:179], s[72:73], 0, v[164:165]
	s_mov_b32 m0, s33
	s_nop 0
	global_load_lds_dwordx4 v[178:179], off
	s_mov_b32 m0, s69
	s_nop 0
	global_load_lds_dwordx4 v[180:181], off
	s_waitcnt vmcnt(24)
	s_waitcnt lgkmcnt(0)
	s_barrier
	v_mfma_scale_f32_16x16x128_f8f6f4 v[94:97], v[26:33], v[190:197], 0, v187, v188 op_sel_hi:[0,0,0]
	v_mfma_scale_f32_16x16x128_f8f6f4 v[90:93], v[18:25], v[190:197], 0, v187, v188 op_sel_hi:[0,0,0]
	v_mfma_scale_f32_16x16x128_f8f6f4 v[86:89], v[26:33], v[198:205], 0, v187, v188 op_sel_hi:[0,0,0]
	v_mfma_scale_f32_16x16x128_f8f6f4 v[78:81], v[18:25], v[198:205], 0, v187, v188 op_sel_hi:[0,0,0]
	v_mfma_scale_f32_16x16x128_f8f6f4 v[70:73], v[26:33], v[206:213], 0, v187, v188 op_sel_hi:[0,0,0]
	v_mfma_scale_f32_16x16x128_f8f6f4 v[62:65], v[18:25], v[206:213], 0, v187, v188 op_sel_hi:[0,0,0]
	v_mfma_scale_f32_16x16x128_f8f6f4 v[54:57], v[26:33], v[220:227], 0, v187, v188 op_sel_hi:[0,0,0]
	v_mfma_scale_f32_16x16x128_f8f6f4 v[46:49], v[18:25], v[220:227], 0, v187, v188 op_sel_hi:[0,0,0]
	v_mfma_scale_f32_16x16x128_f8f6f4 v[82:85], v[10:17], v[190:197], 0, v187, v188 op_sel_hi:[0,0,0]
	v_mfma_scale_f32_16x16x128_f8f6f4 v[74:77], v[2:9], v[190:197], 0, v187, v188 op_sel_hi:[0,0,0]
	v_mfma_scale_f32_16x16x128_f8f6f4 v[66:69], v[10:17], v[198:205], 0, v187, v188 op_sel_hi:[0,0,0]
	v_mfma_scale_f32_16x16x128_f8f6f4 v[58:61], v[2:9], v[198:205], 0, v187, v188 op_sel_hi:[0,0,0]
	v_mfma_scale_f32_16x16x128_f8f6f4 v[50:53], v[10:17], v[206:213], 0, v187, v188 op_sel_hi:[0,0,0]
	v_mfma_scale_f32_16x16x128_f8f6f4 v[42:45], v[2:9], v[206:213], 0, v187, v188 op_sel_hi:[0,0,0]
	v_mfma_scale_f32_16x16x128_f8f6f4 v[38:41], v[10:17], v[220:227], 0, v187, v188 op_sel_hi:[0,0,0]
	v_mfma_scale_f32_16x16x128_f8f6f4 v[34:37], v[2:9], v[220:227], 0, v187, v188 op_sel_hi:[0,0,0]
	s_barrier
	s_add_i32 s74, 0, 0x18000
	s_add_i32 s75, 0, 0x1c000
	v_add_u32_e32 v14, s74, v183
	v_add_u32_e32 v30, s75, v183
	ds_read_b128 v[2:5], v14
	ds_read_b128 v[6:9], v14 offset:1024
	ds_read_b128 v[10:13], v14 offset:2048
	ds_read_b128 v[14:17], v14 offset:3072
	ds_read_b128 v[18:21], v30
	ds_read_b128 v[22:25], v30 offset:1024
	ds_read_b128 v[26:29], v30 offset:2048
	ds_read_b128 v[30:33], v30 offset:3072
	s_add_u32 s26, s72, 0x40000
	s_addc_u32 s27, s73, 0
	s_mov_b32 m0, s83
	v_lshl_add_u64 v[214:215], s[26:27], 0, v[164:165]
	ds_read_b128 v[190:193], v186 offset:32768
	ds_read_b128 v[194:197], v186 offset:33792
	ds_read_b128 v[198:201], v186 offset:34816
	ds_read_b128 v[202:205], v186 offset:35840
	ds_read_b128 v[206:209], v186 offset:36864
	ds_read_b128 v[210:213], v186 offset:37888
	ds_read_b128 v[220:223], v186 offset:38912
	ds_read_b128 v[224:227], v186 offset:39936
	global_load_lds_dwordx4 v[214:215], off
	v_lshl_add_u64 v[214:215], s[26:27], 0, v[166:167]
	s_mov_b32 m0, s84
	s_nop 0
	global_load_lds_dwordx4 v[214:215], off
	s_waitcnt vmcnt(8)
	s_waitcnt lgkmcnt(0)
	s_barrier
	v_mfma_scale_f32_16x16x128_f8f6f4 v[158:161], v[2:9], v[190:197], v[158:161], v187, v188 op_sel_hi:[0,0,0]
	v_mfma_scale_f32_16x16x128_f8f6f4 v[154:157], v[10:17], v[190:197], v[154:157], v187, v188 op_sel_hi:[0,0,0]
	v_mfma_scale_f32_16x16x128_f8f6f4 v[150:153], v[2:9], v[198:205], v[150:153], v187, v188 op_sel_hi:[0,0,0]
	v_mfma_scale_f32_16x16x128_f8f6f4 v[142:145], v[10:17], v[198:205], v[142:145], v187, v188 op_sel_hi:[0,0,0]
	v_mfma_scale_f32_16x16x128_f8f6f4 v[134:137], v[2:9], v[206:213], v[134:137], v187, v188 op_sel_hi:[0,0,0]
	v_mfma_scale_f32_16x16x128_f8f6f4 v[126:129], v[10:17], v[206:213], v[126:129], v187, v188 op_sel_hi:[0,0,0]
	v_mfma_scale_f32_16x16x128_f8f6f4 v[118:121], v[2:9], v[220:227], v[118:121], v187, v188 op_sel_hi:[0,0,0]
	v_mfma_scale_f32_16x16x128_f8f6f4 v[110:113], v[10:17], v[220:227], v[110:113], v187, v188 op_sel_hi:[0,0,0]
	v_mfma_scale_f32_16x16x128_f8f6f4 v[146:149], v[18:25], v[190:197], v[146:149], v187, v188 op_sel_hi:[0,0,0]
	v_mfma_scale_f32_16x16x128_f8f6f4 v[138:141], v[26:33], v[190:197], v[138:141], v187, v188 op_sel_hi:[0,0,0]
	v_mfma_scale_f32_16x16x128_f8f6f4 v[130:133], v[18:25], v[198:205], v[130:133], v187, v188 op_sel_hi:[0,0,0]
	v_mfma_scale_f32_16x16x128_f8f6f4 v[122:125], v[26:33], v[198:205], v[122:125], v187, v188 op_sel_hi:[0,0,0]
	v_mfma_scale_f32_16x16x128_f8f6f4 v[114:117], v[18:25], v[206:213], v[114:117], v187, v188 op_sel_hi:[0,0,0]
	v_mfma_scale_f32_16x16x128_f8f6f4 v[106:109], v[26:33], v[206:213], v[106:109], v187, v188 op_sel_hi:[0,0,0]
	v_mfma_scale_f32_16x16x128_f8f6f4 v[102:105], v[18:25], v[220:227], v[102:105], v187, v188 op_sel_hi:[0,0,0]
	v_mfma_scale_f32_16x16x128_f8f6f4 v[98:101], v[26:33], v[220:227], v[98:101], v187, v188 op_sel_hi:[0,0,0]
	s_barrier
	s_add_i32 s26, s74, s80
	v_lshl_add_u64 v[214:215], v[176:177], 0, s[16:17]
	s_mov_b32 m0, s26
	ds_read_b128 v[190:193], v186 offset:49152
	ds_read_b128 v[194:197], v186 offset:50176
	ds_read_b128 v[198:201], v186 offset:51200
	ds_read_b128 v[202:205], v186 offset:52224
	ds_read_b128 v[206:209], v186 offset:53248
	ds_read_b128 v[210:213], v186 offset:54272
	ds_read_b128 v[220:223], v186 offset:55296
	ds_read_b128 v[224:227], v186 offset:56320
	global_load_lds_dwordx4 v[214:215], off
	v_lshl_add_u64 v[214:215], v[176:177], 0, s[18:19]
	s_add_i32 m0, s26, 0x2000
	s_add_i32 s26, s75, s80
	global_load_lds_dwordx4 v[214:215], off
	v_lshl_add_u64 v[214:215], v[176:177], 0, s[22:23]
	s_mov_b32 m0, s26
	v_lshl_add_u64 v[176:177], v[176:177], 0, s[24:25]
	global_load_lds_dwordx4 v[214:215], off
	s_add_i32 m0, s26, 0x2000
	s_nop 0
	global_load_lds_dwordx4 v[176:177], off
	v_lshl_add_u64 v[176:177], v[178:179], 0, s[20:21]
	s_mov_b32 m0, s86
	s_nop 0
	global_load_lds_dwordx4 v[176:177], off
	v_lshl_add_u64 v[176:177], v[180:181], 0, s[20:21]
	s_mov_b32 m0, s87
	s_nop 0
	global_load_lds_dwordx4 v[176:177], off
	s_waitcnt vmcnt(8)
	s_waitcnt lgkmcnt(0)
	s_barrier
	v_mfma_scale_f32_16x16x128_f8f6f4 v[94:97], v[2:9], v[190:197], v[94:97], v187, v188 op_sel_hi:[0,0,0]
	v_mfma_scale_f32_16x16x128_f8f6f4 v[90:93], v[10:17], v[190:197], v[90:93], v187, v188 op_sel_hi:[0,0,0]
	v_mfma_scale_f32_16x16x128_f8f6f4 v[86:89], v[2:9], v[198:205], v[86:89], v187, v188 op_sel_hi:[0,0,0]
	v_mfma_scale_f32_16x16x128_f8f6f4 v[78:81], v[10:17], v[198:205], v[78:81], v187, v188 op_sel_hi:[0,0,0]
	v_mfma_scale_f32_16x16x128_f8f6f4 v[70:73], v[2:9], v[206:213], v[70:73], v187, v188 op_sel_hi:[0,0,0]
	v_mfma_scale_f32_16x16x128_f8f6f4 v[62:65], v[10:17], v[206:213], v[62:65], v187, v188 op_sel_hi:[0,0,0]
	v_mfma_scale_f32_16x16x128_f8f6f4 v[54:57], v[2:9], v[220:227], v[54:57], v187, v188 op_sel_hi:[0,0,0]
	v_mfma_scale_f32_16x16x128_f8f6f4 v[46:49], v[10:17], v[220:227], v[46:49], v187, v188 op_sel_hi:[0,0,0]
	v_mfma_scale_f32_16x16x128_f8f6f4 v[82:85], v[18:25], v[190:197], v[82:85], v187, v188 op_sel_hi:[0,0,0]
	v_mfma_scale_f32_16x16x128_f8f6f4 v[74:77], v[26:33], v[190:197], v[74:77], v187, v188 op_sel_hi:[0,0,0]
	v_mfma_scale_f32_16x16x128_f8f6f4 v[66:69], v[18:25], v[198:205], v[66:69], v187, v188 op_sel_hi:[0,0,0]
	v_mfma_scale_f32_16x16x128_f8f6f4 v[58:61], v[26:33], v[198:205], v[58:61], v187, v188 op_sel_hi:[0,0,0]
	v_mfma_scale_f32_16x16x128_f8f6f4 v[50:53], v[18:25], v[206:213], v[50:53], v187, v188 op_sel_hi:[0,0,0]
	v_mfma_scale_f32_16x16x128_f8f6f4 v[42:45], v[26:33], v[206:213], v[42:45], v187, v188 op_sel_hi:[0,0,0]
	v_mfma_scale_f32_16x16x128_f8f6f4 v[38:41], v[18:25], v[220:227], v[38:41], v187, v188 op_sel_hi:[0,0,0]
	v_mfma_scale_f32_16x16x128_f8f6f4 v[34:37], v[26:33], v[220:227], v[34:37], v187, v188 op_sel_hi:[0,0,0]
	s_barrier
	s_add_i32 s94, s94, 2
	s_add_u32 s92, s92, 0x10000
	s_addc_u32 s93, s93, 0
	s_add_u32 s70, s70, 0x100
	s_addc_u32 s71, s71, 0
	s_cmp_gt_u32 s94, 13

.LBB0_659:
	s_ashr_i32 s45, s44, 31
	s_lshl_b64 s[26:27], s[44:45], 20
	v_readlane_b32 s50, v254, 58
	v_readlane_b32 s51, v254, 59
	s_add_u32 s50, s50, s26
	s_addc_u32 s51, s51, s27
	s_and_b64 s[26:27], s[0:1], exec
	s_cselect_b32 s45, s51, s61
	s_cselect_b32 s72, s50, s60
	s_ashr_i32 s41, s40, 31
	s_lshl_b64 s[26:27], s[40:41], 20
	s_add_u32 s54, s3, s26
	s_addc_u32 s55, s33, s27
	s_and_b64 s[26:27], s[0:1], exec
	s_cselect_b32 s41, s55, s59
	s_cselect_b32 s73, s54, s58
	s_add_u32 s74, s58, 0x10000
	s_addc_u32 s75, s59, 0
	s_add_u32 s58, s60, 0x80080
	s_addc_u32 s59, s61, 0
	s_mov_b32 s80, -2
	ds_read_b128 v[130:133], v222
	ds_read_b128 v[134:137], v222 offset:1024
	ds_read_b128 v[138:141], v222 offset:2048
	ds_read_b128 v[142:145], v222 offset:3072
	ds_read_b128 v[146:149], v223
	ds_read_b128 v[150:153], v223 offset:1024
	ds_read_b128 v[154:157], v223 offset:2048
	ds_read_b128 v[158:161], v223 offset:3072
	s_add_u32 s26, s58, 0xfff80080
	s_addc_u32 s27, s59, -1
	s_cmp_eq_u32 s80, 28
	s_cselect_b32 s61, s45, s27
	s_cselect_b32 s60, s72, s26
	s_cselect_b32 s27, s41, s75
	s_cselect_b32 s26, s73, s74
	v_lshl_add_u64 v[208:209], s[58:59], 0, v[200:201]
	s_add_i32 m0, s57, 0xc000
	ds_read_b128 v[162:165], v224
	ds_read_b128 v[166:169], v224 offset:1024
	ds_read_b128 v[170:173], v224 offset:2048
	ds_read_b128 v[174:177], v224 offset:3072
	ds_read_b128 v[178:181], v224 offset:4096
	ds_read_b128 v[182:185], v224 offset:5120
	ds_read_b128 v[186:189], v224 offset:6144
	ds_read_b128 v[190:193], v224 offset:7168
	global_load_lds_dwordx4 v[208:209], off
	v_lshl_add_u64 v[208:209], s[58:59], 0, v[202:203]
	s_add_i32 m0, s57, 0xe000
	s_nop 0
	global_load_lds_dwordx4 v[208:209], off
	s_waitcnt vmcnt(8)
	s_waitcnt lgkmcnt(0)
	s_barrier
	v_mfma_f32_16x16x32_bf16 v[126:129], v[130:133], v[162:165], 0
	v_mfma_f32_16x16x32_bf16 v[122:125], v[138:141], v[162:165], 0
	v_mfma_f32_16x16x32_bf16 v[118:121], v[130:133], v[170:173], 0
	v_mfma_f32_16x16x32_bf16 v[114:117], v[138:141], v[170:173], 0
	v_mfma_f32_16x16x32_bf16 v[110:113], v[130:133], v[178:181], 0
	v_mfma_f32_16x16x32_bf16 v[102:105], v[138:141], v[178:181], 0
	v_mfma_f32_16x16x32_bf16 v[94:97], v[130:133], v[186:189], 0
	v_mfma_f32_16x16x32_bf16 v[74:77], v[138:141], v[186:189], 0
	v_mfma_f32_16x16x32_bf16 v[126:129], v[134:137], v[166:169], v[126:129]
	v_mfma_f32_16x16x32_bf16 v[122:125], v[142:145], v[166:169], v[122:125]
	v_mfma_f32_16x16x32_bf16 v[118:121], v[134:137], v[174:177], v[118:121]
	v_mfma_f32_16x16x32_bf16 v[114:117], v[142:145], v[174:177], v[114:117]
	v_mfma_f32_16x16x32_bf16 v[110:113], v[134:137], v[182:185], v[110:113]
	v_mfma_f32_16x16x32_bf16 v[102:105], v[142:145], v[182:185], v[102:105]
	v_mfma_f32_16x16x32_bf16 v[94:97], v[134:137], v[190:193], v[94:97]
	v_mfma_f32_16x16x32_bf16 v[74:77], v[142:145], v[190:193], v[74:77]
	v_mfma_f32_16x16x32_bf16 v[106:109], v[146:149], v[162:165], 0
	v_mfma_f32_16x16x32_bf16 v[98:101], v[154:157], v[162:165], 0
	v_mfma_f32_16x16x32_bf16 v[90:93], v[146:149], v[170:173], 0
	v_mfma_f32_16x16x32_bf16 v[86:89], v[154:157], v[170:173], 0
	v_mfma_f32_16x16x32_bf16 v[82:85], v[146:149], v[178:181], 0
	v_mfma_f32_16x16x32_bf16 v[78:81], v[154:157], v[178:181], 0
	v_mfma_f32_16x16x32_bf16 v[70:73], v[146:149], v[186:189], 0
	v_mfma_f32_16x16x32_bf16 v[66:69], v[154:157], v[186:189], 0
	v_mfma_f32_16x16x32_bf16 v[106:109], v[150:153], v[166:169], v[106:109]
	v_mfma_f32_16x16x32_bf16 v[98:101], v[158:161], v[166:169], v[98:101]
	v_mfma_f32_16x16x32_bf16 v[90:93], v[150:153], v[174:177], v[90:93]
	v_mfma_f32_16x16x32_bf16 v[86:89], v[158:161], v[174:177], v[86:89]
	v_mfma_f32_16x16x32_bf16 v[82:85], v[150:153], v[182:185], v[82:85]
	v_mfma_f32_16x16x32_bf16 v[78:81], v[158:161], v[182:185], v[78:81]
	v_mfma_f32_16x16x32_bf16 v[70:73], v[150:153], v[190:193], v[70:73]
	v_mfma_f32_16x16x32_bf16 v[66:69], v[158:161], v[190:193], v[66:69]
	s_barrier
	v_lshl_add_u64 v[208:209], s[26:27], 0, v[194:195]
	s_add_i32 s26, s70, s35
	s_mov_b32 m0, s26
	ds_read_b128 v[162:165], v224 offset:16384
	ds_read_b128 v[166:169], v224 offset:17408
	ds_read_b128 v[170:173], v224 offset:18432
	ds_read_b128 v[174:177], v224 offset:19456
	ds_read_b128 v[178:181], v224 offset:20480
	ds_read_b128 v[182:185], v224 offset:21504
	ds_read_b128 v[186:189], v224 offset:22528
	ds_read_b128 v[190:193], v224 offset:23552
	global_load_lds_dwordx4 v[208:209], off
	v_lshl_add_u64 v[210:211], v[208:209], 0, s[6:7]
	s_add_i32 m0, s26, 0x2000
	s_add_i32 s26, s71, s35
	global_load_lds_dwordx4 v[210:211], off
	v_lshl_add_u64 v[210:211], v[208:209], 0, s[8:9]
	s_mov_b32 m0, s26
	v_lshl_add_u64 v[212:213], s[60:61], 0, v[198:199]
	global_load_lds_dwordx4 v[210:211], off
	v_lshl_add_u64 v[210:211], v[208:209], 0, s[10:11]
	s_add_i32 m0, s26, 0x2000
	s_nop 0
	global_load_lds_dwordx4 v[210:211], off
	v_lshl_add_u64 v[210:211], s[60:61], 0, v[196:197]
	s_mov_b32 m0, s57
	s_nop 0
	global_load_lds_dwordx4 v[210:211], off
	s_mov_b32 m0, s63
	s_nop 0
	global_load_lds_dwordx4 v[212:213], off
	s_waitcnt vmcnt(8)
	s_waitcnt lgkmcnt(0)
	s_barrier
	v_mfma_f32_16x16x32_bf16 v[62:65], v[130:133], v[162:165], 0
	v_mfma_f32_16x16x32_bf16 v[58:61], v[138:141], v[162:165], 0
	v_mfma_f32_16x16x32_bf16 v[54:57], v[130:133], v[170:173], 0
	v_mfma_f32_16x16x32_bf16 v[50:53], v[138:141], v[170:173], 0
	v_mfma_f32_16x16x32_bf16 v[46:49], v[130:133], v[178:181], 0
	v_mfma_f32_16x16x32_bf16 v[38:41], v[138:141], v[178:181], 0
	v_mfma_f32_16x16x32_bf16 v[30:33], v[130:133], v[186:189], 0
	v_mfma_f32_16x16x32_bf16 v[10:13], v[138:141], v[186:189], 0
	v_mfma_f32_16x16x32_bf16 v[62:65], v[134:137], v[166:169], v[62:65]
	v_mfma_f32_16x16x32_bf16 v[58:61], v[142:145], v[166:169], v[58:61]
	v_mfma_f32_16x16x32_bf16 v[54:57], v[134:137], v[174:177], v[54:57]
	v_mfma_f32_16x16x32_bf16 v[50:53], v[142:145], v[174:177], v[50:53]
	v_mfma_f32_16x16x32_bf16 v[46:49], v[134:137], v[182:185], v[46:49]
	v_mfma_f32_16x16x32_bf16 v[38:41], v[142:145], v[182:185], v[38:41]
	v_mfma_f32_16x16x32_bf16 v[30:33], v[134:137], v[190:193], v[30:33]
	v_mfma_f32_16x16x32_bf16 v[10:13], v[142:145], v[190:193], v[10:13]
	v_mfma_f32_16x16x32_bf16 v[42:45], v[146:149], v[162:165], 0
	v_mfma_f32_16x16x32_bf16 v[34:37], v[154:157], v[162:165], 0
	v_mfma_f32_16x16x32_bf16 v[26:29], v[146:149], v[170:173], 0
	v_mfma_f32_16x16x32_bf16 v[22:25], v[154:157], v[170:173], 0
	v_mfma_f32_16x16x32_bf16 v[18:21], v[146:149], v[178:181], 0
	v_mfma_f32_16x16x32_bf16 v[14:17], v[154:157], v[178:181], 0
	v_mfma_f32_16x16x32_bf16 v[6:9], v[146:149], v[186:189], 0
	v_mfma_f32_16x16x32_bf16 v[2:5], v[154:157], v[186:189], 0
	v_mfma_f32_16x16x32_bf16 v[42:45], v[150:153], v[166:169], v[42:45]
	v_mfma_f32_16x16x32_bf16 v[34:37], v[158:161], v[166:169], v[34:37]
	v_mfma_f32_16x16x32_bf16 v[26:29], v[150:153], v[174:177], v[26:29]
	v_mfma_f32_16x16x32_bf16 v[22:25], v[158:161], v[174:177], v[22:25]
	v_mfma_f32_16x16x32_bf16 v[18:21], v[150:153], v[182:185], v[18:21]
	v_mfma_f32_16x16x32_bf16 v[14:17], v[158:161], v[182:185], v[14:17]
	v_mfma_f32_16x16x32_bf16 v[6:9], v[150:153], v[190:193], v[6:9]
	v_mfma_f32_16x16x32_bf16 v[2:5], v[158:161], v[190:193], v[2:5]
	s_barrier
	s_add_i32 s81, 0, 0x18000
	s_add_i32 s82, 0, 0x1c000
	v_add_u32_e32 v142, s81, v220
	v_add_u32_e32 v158, s82, v220
	ds_read_b128 v[130:133], v142
	ds_read_b128 v[134:137], v142 offset:1024
	ds_read_b128 v[138:141], v142 offset:2048
	ds_read_b128 v[142:145], v142 offset:3072
	ds_read_b128 v[146:149], v158
	ds_read_b128 v[150:153], v158 offset:1024
	ds_read_b128 v[154:157], v158 offset:2048
	ds_read_b128 v[158:161], v158 offset:3072
	s_add_u32 s26, s60, 0x80000
	s_addc_u32 s27, s61, 0
	s_mov_b32 m0, s64
	v_lshl_add_u64 v[214:215], s[26:27], 0, v[196:197]
	ds_read_b128 v[162:165], v224 offset:32768
	ds_read_b128 v[166:169], v224 offset:33792
	ds_read_b128 v[170:173], v224 offset:34816
	ds_read_b128 v[174:177], v224 offset:35840
	ds_read_b128 v[178:181], v224 offset:36864
	ds_read_b128 v[182:185], v224 offset:37888
	ds_read_b128 v[186:189], v224 offset:38912
	ds_read_b128 v[190:193], v224 offset:39936
	global_load_lds_dwordx4 v[214:215], off
	v_lshl_add_u64 v[214:215], s[26:27], 0, v[198:199]
	s_mov_b32 m0, s65
	s_nop 0
	global_load_lds_dwordx4 v[214:215], off
	s_waitcnt vmcnt(8)
	s_waitcnt lgkmcnt(0)
	s_barrier
	v_mfma_f32_16x16x32_bf16 v[126:129], v[130:133], v[162:165], v[126:129]
	v_mfma_f32_16x16x32_bf16 v[122:125], v[138:141], v[162:165], v[122:125]
	v_mfma_f32_16x16x32_bf16 v[118:121], v[130:133], v[170:173], v[118:121]
	v_mfma_f32_16x16x32_bf16 v[114:117], v[138:141], v[170:173], v[114:117]
	v_mfma_f32_16x16x32_bf16 v[110:113], v[130:133], v[178:181], v[110:113]
	v_mfma_f32_16x16x32_bf16 v[102:105], v[138:141], v[178:181], v[102:105]
	v_mfma_f32_16x16x32_bf16 v[94:97], v[130:133], v[186:189], v[94:97]
	v_mfma_f32_16x16x32_bf16 v[74:77], v[138:141], v[186:189], v[74:77]
	v_mfma_f32_16x16x32_bf16 v[126:129], v[134:137], v[166:169], v[126:129]
	v_mfma_f32_16x16x32_bf16 v[122:125], v[142:145], v[166:169], v[122:125]
	v_mfma_f32_16x16x32_bf16 v[118:121], v[134:137], v[174:177], v[118:121]
	v_mfma_f32_16x16x32_bf16 v[114:117], v[142:145], v[174:177], v[114:117]
	v_mfma_f32_16x16x32_bf16 v[110:113], v[134:137], v[182:185], v[110:113]
	v_mfma_f32_16x16x32_bf16 v[102:105], v[142:145], v[182:185], v[102:105]
	v_mfma_f32_16x16x32_bf16 v[94:97], v[134:137], v[190:193], v[94:97]
	v_mfma_f32_16x16x32_bf16 v[74:77], v[142:145], v[190:193], v[74:77]
	v_mfma_f32_16x16x32_bf16 v[106:109], v[146:149], v[162:165], v[106:109]
	v_mfma_f32_16x16x32_bf16 v[98:101], v[154:157], v[162:165], v[98:101]
	v_mfma_f32_16x16x32_bf16 v[90:93], v[146:149], v[170:173], v[90:93]
	v_mfma_f32_16x16x32_bf16 v[86:89], v[154:157], v[170:173], v[86:89]
	v_mfma_f32_16x16x32_bf16 v[82:85], v[146:149], v[178:181], v[82:85]
	v_mfma_f32_16x16x32_bf16 v[78:81], v[154:157], v[178:181], v[78:81]
	v_mfma_f32_16x16x32_bf16 v[70:73], v[146:149], v[186:189], v[70:73]
	v_mfma_f32_16x16x32_bf16 v[66:69], v[154:157], v[186:189], v[66:69]
	v_mfma_f32_16x16x32_bf16 v[106:109], v[150:153], v[166:169], v[106:109]
	v_mfma_f32_16x16x32_bf16 v[98:101], v[158:161], v[166:169], v[98:101]
	v_mfma_f32_16x16x32_bf16 v[90:93], v[150:153], v[174:177], v[90:93]
	v_mfma_f32_16x16x32_bf16 v[86:89], v[158:161], v[174:177], v[86:89]
	v_mfma_f32_16x16x32_bf16 v[82:85], v[150:153], v[182:185], v[82:85]
	v_mfma_f32_16x16x32_bf16 v[78:81], v[158:161], v[182:185], v[78:81]
	v_mfma_f32_16x16x32_bf16 v[70:73], v[150:153], v[190:193], v[70:73]
	v_mfma_f32_16x16x32_bf16 v[66:69], v[158:161], v[190:193], v[66:69]
	s_barrier
	s_add_i32 s26, s81, s35
	v_lshl_add_u64 v[214:215], v[208:209], 0, s[14:15]
	s_mov_b32 m0, s26
	ds_read_b128 v[162:165], v224 offset:49152
	ds_read_b128 v[166:169], v224 offset:50176
	ds_read_b128 v[170:173], v224 offset:51200
	ds_read_b128 v[174:177], v224 offset:52224
	ds_read_b128 v[178:181], v224 offset:53248
	ds_read_b128 v[182:185], v224 offset:54272
	ds_read_b128 v[186:189], v224 offset:55296
	ds_read_b128 v[190:193], v224 offset:56320
	global_load_lds_dwordx4 v[214:215], off
	v_lshl_add_u64 v[214:215], v[208:209], 0, s[16:17]
	s_add_i32 m0, s26, 0x2000
	s_add_i32 s26, s82, s35
	global_load_lds_dwordx4 v[214:215], off
	v_lshl_add_u64 v[214:215], v[208:209], 0, s[20:21]
	s_mov_b32 m0, s26
	v_lshl_add_u64 v[208:209], v[208:209], 0, s[22:23]
	global_load_lds_dwordx4 v[214:215], off
	s_add_i32 m0, s26, 0x2000
	s_nop 0
	global_load_lds_dwordx4 v[208:209], off
	v_lshl_add_u64 v[208:209], v[210:211], 0, s[18:19]
	s_mov_b32 m0, s67
	s_nop 0
	global_load_lds_dwordx4 v[208:209], off
	v_lshl_add_u64 v[208:209], v[212:213], 0, s[18:19]
	s_mov_b32 m0, s68
	s_nop 0
	global_load_lds_dwordx4 v[208:209], off
	s_waitcnt vmcnt(8)
	s_waitcnt lgkmcnt(0)
	s_barrier
	v_mfma_f32_16x16x32_bf16 v[62:65], v[130:133], v[162:165], v[62:65]
	v_mfma_f32_16x16x32_bf16 v[58:61], v[138:141], v[162:165], v[58:61]
	v_mfma_f32_16x16x32_bf16 v[54:57], v[130:133], v[170:173], v[54:57]
	v_mfma_f32_16x16x32_bf16 v[50:53], v[138:141], v[170:173], v[50:53]
	v_mfma_f32_16x16x32_bf16 v[46:49], v[130:133], v[178:181], v[46:49]
	v_mfma_f32_16x16x32_bf16 v[38:41], v[138:141], v[178:181], v[38:41]
	v_mfma_f32_16x16x32_bf16 v[30:33], v[130:133], v[186:189], v[30:33]
	v_mfma_f32_16x16x32_bf16 v[10:13], v[138:141], v[186:189], v[10:13]
	v_mfma_f32_16x16x32_bf16 v[62:65], v[134:137], v[166:169], v[62:65]
	v_mfma_f32_16x16x32_bf16 v[58:61], v[142:145], v[166:169], v[58:61]
	v_mfma_f32_16x16x32_bf16 v[54:57], v[134:137], v[174:177], v[54:57]
	v_mfma_f32_16x16x32_bf16 v[50:53], v[142:145], v[174:177], v[50:53]
	v_mfma_f32_16x16x32_bf16 v[46:49], v[134:137], v[182:185], v[46:49]
	v_mfma_f32_16x16x32_bf16 v[38:41], v[142:145], v[182:185], v[38:41]
	v_mfma_f32_16x16x32_bf16 v[30:33], v[134:137], v[190:193], v[30:33]
	v_mfma_f32_16x16x32_bf16 v[10:13], v[142:145], v[190:193], v[10:13]
	v_mfma_f32_16x16x32_bf16 v[42:45], v[146:149], v[162:165], v[42:45]
	v_mfma_f32_16x16x32_bf16 v[34:37], v[154:157], v[162:165], v[34:37]
	v_mfma_f32_16x16x32_bf16 v[26:29], v[146:149], v[170:173], v[26:29]
	v_mfma_f32_16x16x32_bf16 v[22:25], v[154:157], v[170:173], v[22:25]
	v_mfma_f32_16x16x32_bf16 v[18:21], v[146:149], v[178:181], v[18:21]
	v_mfma_f32_16x16x32_bf16 v[14:17], v[154:157], v[178:181], v[14:17]
	v_mfma_f32_16x16x32_bf16 v[6:9], v[146:149], v[186:189], v[6:9]
	v_mfma_f32_16x16x32_bf16 v[2:5], v[154:157], v[186:189], v[2:5]
	v_mfma_f32_16x16x32_bf16 v[42:45], v[150:153], v[166:169], v[42:45]
	v_mfma_f32_16x16x32_bf16 v[34:37], v[158:161], v[166:169], v[34:37]
	v_mfma_f32_16x16x32_bf16 v[26:29], v[150:153], v[174:177], v[26:29]
	v_mfma_f32_16x16x32_bf16 v[22:25], v[158:161], v[174:177], v[22:25]
	v_mfma_f32_16x16x32_bf16 v[18:21], v[150:153], v[182:185], v[18:21]
	v_mfma_f32_16x16x32_bf16 v[14:17], v[158:161], v[182:185], v[14:17]
	v_mfma_f32_16x16x32_bf16 v[6:9], v[150:153], v[190:193], v[6:9]
	v_mfma_f32_16x16x32_bf16 v[2:5], v[158:161], v[190:193], v[2:5]
	s_barrier
	s_add_i32 s80, s80, 2
	s_add_u32 s74, s74, 0x10000
	s_addc_u32 s75, s75, 0
	s_add_u32 s58, s58, 0x100
	s_addc_u32 s59, s59, 0
	s_cmp_gt_u32 s80, 29

.LBB0_782:
	s_ashr_i32 s55, s54, 31
	s_lshl_b64 s[26:27], s[54:55], 20
	v_readlane_b32 s56, v254, 56
	v_readlane_b32 s57, v254, 57
	s_add_u32 s56, s56, s26
	s_addc_u32 s57, s57, s27
	s_and_b64 s[26:27], s[0:1], exec
	s_cselect_b32 s55, s57, s65
	s_cselect_b32 s81, s56, s64
	s_ashr_i32 s53, s52, 31
	s_lshl_b64 s[26:27], s[52:53], 20
	s_add_u32 s58, s3, s26
	s_addc_u32 s59, s33, s27
	s_and_b64 s[26:27], s[0:1], exec
	s_cselect_b32 s53, s59, s63
	s_cselect_b32 s82, s58, s62
	s_add_u32 s83, s62, 0x10000
	s_addc_u32 s84, s63, 0
	s_add_u32 s62, s64, 0x80080
	s_addc_u32 s63, s65, 0
	s_mov_b32 s85, -2
	ds_read_b128 v[144:147], v151
	ds_read_b128 v[156:159], v151 offset:1024
	ds_read_b128 v[160:163], v151 offset:2048
	ds_read_b128 v[164:167], v151 offset:3072
	ds_read_b128 v[168:171], v152
	ds_read_b128 v[172:175], v152 offset:1024
	ds_read_b128 v[176:179], v152 offset:2048
	ds_read_b128 v[180:183], v152 offset:3072
	s_add_u32 s26, s62, 0xfff80080
	s_addc_u32 s27, s63, -1
	s_cmp_eq_u32 s85, 28
	s_cselect_b32 s65, s55, s27
	s_cselect_b32 s64, s81, s26
	s_cselect_b32 s27, s53, s84
	s_cselect_b32 s26, s82, s83
	v_lshl_add_u64 v[216:217], s[62:63], 0, v[136:137]
	s_add_i32 m0, s61, 0xc000
	ds_read_b128 v[184:187], v153
	ds_read_b128 v[188:191], v153 offset:1024
	ds_read_b128 v[192:195], v153 offset:2048
	ds_read_b128 v[196:199], v153 offset:3072
	ds_read_b128 v[200:203], v153 offset:4096
	ds_read_b128 v[204:207], v153 offset:5120
	ds_read_b128 v[208:211], v153 offset:6144
	ds_read_b128 v[212:215], v153 offset:7168
	global_load_lds_dwordx4 v[216:217], off
	v_lshl_add_u64 v[216:217], s[62:63], 0, v[138:139]
	s_add_i32 m0, s61, 0xe000
	s_nop 0
	global_load_lds_dwordx4 v[216:217], off
	s_waitcnt vmcnt(16)
	s_waitcnt lgkmcnt(0)
	s_barrier
	v_mfma_f32_16x16x32_bf16 v[126:129], v[144:147], v[184:187], 0
	v_mfma_f32_16x16x32_bf16 v[118:121], v[160:163], v[184:187], 0
	v_mfma_f32_16x16x32_bf16 v[110:113], v[144:147], v[192:195], 0
	v_mfma_f32_16x16x32_bf16 v[102:105], v[160:163], v[192:195], 0
	v_mfma_f32_16x16x32_bf16 v[94:97], v[144:147], v[200:203], 0
	v_mfma_f32_16x16x32_bf16 v[86:89], v[160:163], v[200:203], 0
	v_mfma_f32_16x16x32_bf16 v[78:81], v[144:147], v[208:211], 0
	v_mfma_f32_16x16x32_bf16 v[70:73], v[160:163], v[208:211], 0
	v_mfma_f32_16x16x32_bf16 v[126:129], v[156:159], v[188:191], v[126:129]
	v_mfma_f32_16x16x32_bf16 v[118:121], v[164:167], v[188:191], v[118:121]
	v_mfma_f32_16x16x32_bf16 v[110:113], v[156:159], v[196:199], v[110:113]
	v_mfma_f32_16x16x32_bf16 v[102:105], v[164:167], v[196:199], v[102:105]
	v_mfma_f32_16x16x32_bf16 v[94:97], v[156:159], v[204:207], v[94:97]
	v_mfma_f32_16x16x32_bf16 v[86:89], v[164:167], v[204:207], v[86:89]
	v_mfma_f32_16x16x32_bf16 v[78:81], v[156:159], v[212:215], v[78:81]
	v_mfma_f32_16x16x32_bf16 v[70:73], v[164:167], v[212:215], v[70:73]
	v_mfma_f32_16x16x32_bf16 v[122:125], v[168:171], v[184:187], 0
	v_mfma_f32_16x16x32_bf16 v[114:117], v[176:179], v[184:187], 0
	v_mfma_f32_16x16x32_bf16 v[106:109], v[168:171], v[192:195], 0
	v_mfma_f32_16x16x32_bf16 v[98:101], v[176:179], v[192:195], 0
	v_mfma_f32_16x16x32_bf16 v[90:93], v[168:171], v[200:203], 0
	v_mfma_f32_16x16x32_bf16 v[82:85], v[176:179], v[200:203], 0
	v_mfma_f32_16x16x32_bf16 v[74:77], v[168:171], v[208:211], 0
	v_mfma_f32_16x16x32_bf16 v[66:69], v[176:179], v[208:211], 0
	v_mfma_f32_16x16x32_bf16 v[122:125], v[172:175], v[188:191], v[122:125]
	v_mfma_f32_16x16x32_bf16 v[114:117], v[180:183], v[188:191], v[114:117]
	v_mfma_f32_16x16x32_bf16 v[106:109], v[172:175], v[196:199], v[106:109]
	v_mfma_f32_16x16x32_bf16 v[98:101], v[180:183], v[196:199], v[98:101]
	v_mfma_f32_16x16x32_bf16 v[90:93], v[172:175], v[204:207], v[90:93]
	v_mfma_f32_16x16x32_bf16 v[82:85], v[180:183], v[204:207], v[82:85]
	v_mfma_f32_16x16x32_bf16 v[74:77], v[172:175], v[212:215], v[74:77]
	v_mfma_f32_16x16x32_bf16 v[66:69], v[180:183], v[212:215], v[66:69]
	s_barrier
	v_lshl_add_u64 v[216:217], s[26:27], 0, v[130:131]
	s_add_i32 s26, s73, s35
	s_mov_b32 m0, s26
	ds_read_b128 v[184:187], v153 offset:16384
	ds_read_b128 v[188:191], v153 offset:17408
	ds_read_b128 v[192:195], v153 offset:18432
	ds_read_b128 v[196:199], v153 offset:19456
	ds_read_b128 v[200:203], v153 offset:20480
	ds_read_b128 v[204:207], v153 offset:21504
	ds_read_b128 v[208:211], v153 offset:22528
	ds_read_b128 v[212:215], v153 offset:23552
	global_load_lds_dwordx4 v[216:217], off
	v_lshl_add_u64 v[220:221], v[216:217], 0, s[6:7]
	s_add_i32 m0, s26, 0x2000
	s_add_i32 s26, s74, s35
	global_load_lds_dwordx4 v[220:221], off
	v_lshl_add_u64 v[220:221], v[216:217], 0, s[8:9]
	s_mov_b32 m0, s26
	v_lshl_add_u64 v[222:223], s[64:65], 0, v[134:135]
	global_load_lds_dwordx4 v[220:221], off
	v_lshl_add_u64 v[220:221], v[216:217], 0, s[10:11]
	s_add_i32 m0, s26, 0x2000
	s_nop 0
	global_load_lds_dwordx4 v[220:221], off
	v_lshl_add_u64 v[220:221], s[64:65], 0, v[132:133]
	s_mov_b32 m0, s61
	s_nop 0
	global_load_lds_dwordx4 v[220:221], off
	s_mov_b32 m0, s66
	s_nop 0
	global_load_lds_dwordx4 v[222:223], off
	s_waitcnt vmcnt(16)
	s_waitcnt lgkmcnt(0)
	s_barrier
	v_mfma_f32_16x16x32_bf16 v[62:65], v[144:147], v[184:187], 0
	v_mfma_f32_16x16x32_bf16 v[54:57], v[160:163], v[184:187], 0
	v_mfma_f32_16x16x32_bf16 v[46:49], v[144:147], v[192:195], 0
	v_mfma_f32_16x16x32_bf16 v[38:41], v[160:163], v[192:195], 0
	v_mfma_f32_16x16x32_bf16 v[30:33], v[144:147], v[200:203], 0
	v_mfma_f32_16x16x32_bf16 v[22:25], v[160:163], v[200:203], 0
	v_mfma_f32_16x16x32_bf16 v[14:17], v[144:147], v[208:211], 0
	v_mfma_f32_16x16x32_bf16 v[6:9], v[160:163], v[208:211], 0
	v_mfma_f32_16x16x32_bf16 v[62:65], v[156:159], v[188:191], v[62:65]
	v_mfma_f32_16x16x32_bf16 v[54:57], v[164:167], v[188:191], v[54:57]
	v_mfma_f32_16x16x32_bf16 v[46:49], v[156:159], v[196:199], v[46:49]
	v_mfma_f32_16x16x32_bf16 v[38:41], v[164:167], v[196:199], v[38:41]
	v_mfma_f32_16x16x32_bf16 v[30:33], v[156:159], v[204:207], v[30:33]
	v_mfma_f32_16x16x32_bf16 v[22:25], v[164:167], v[204:207], v[22:25]
	v_mfma_f32_16x16x32_bf16 v[14:17], v[156:159], v[212:215], v[14:17]
	v_mfma_f32_16x16x32_bf16 v[6:9], v[164:167], v[212:215], v[6:9]
	v_mfma_f32_16x16x32_bf16 v[58:61], v[168:171], v[184:187], 0
	v_mfma_f32_16x16x32_bf16 v[50:53], v[176:179], v[184:187], 0
	v_mfma_f32_16x16x32_bf16 v[42:45], v[168:171], v[192:195], 0
	v_mfma_f32_16x16x32_bf16 v[34:37], v[176:179], v[192:195], 0
	v_mfma_f32_16x16x32_bf16 v[26:29], v[168:171], v[200:203], 0
	v_mfma_f32_16x16x32_bf16 v[18:21], v[176:179], v[200:203], 0
	v_mfma_f32_16x16x32_bf16 v[10:13], v[168:171], v[208:211], 0
	v_mfma_f32_16x16x32_bf16 v[2:5], v[176:179], v[208:211], 0
	v_mfma_f32_16x16x32_bf16 v[58:61], v[172:175], v[188:191], v[58:61]
	v_mfma_f32_16x16x32_bf16 v[50:53], v[180:183], v[188:191], v[50:53]
	v_mfma_f32_16x16x32_bf16 v[42:45], v[172:175], v[196:199], v[42:45]
	v_mfma_f32_16x16x32_bf16 v[34:37], v[180:183], v[196:199], v[34:37]
	v_mfma_f32_16x16x32_bf16 v[26:29], v[172:175], v[204:207], v[26:29]
	v_mfma_f32_16x16x32_bf16 v[18:21], v[180:183], v[204:207], v[18:21]
	v_mfma_f32_16x16x32_bf16 v[10:13], v[172:175], v[212:215], v[10:13]
	v_mfma_f32_16x16x32_bf16 v[2:5], v[180:183], v[212:215], v[2:5]
	s_barrier
	s_add_i32 s86, 0, 0x18000
	v_add_u32_e32 v155, s86, v149
	s_add_i32 s87, 0, 0x1c000
	ds_read_b128 v[144:147], v155
	ds_read_b128 v[156:159], v155 offset:1024
	ds_read_b128 v[160:163], v155 offset:2048
	ds_read_b128 v[164:167], v155 offset:3072
	v_add_u32_e32 v155, s87, v149
	ds_read_b128 v[168:171], v155
	ds_read_b128 v[172:175], v155 offset:1024
	ds_read_b128 v[176:179], v155 offset:2048
	ds_read_b128 v[180:183], v155 offset:3072
	s_add_u32 s26, s64, 0x80000
	s_addc_u32 s27, s65, 0
	s_mov_b32 m0, s67
	v_lshl_add_u64 v[224:225], s[26:27], 0, v[132:133]
	ds_read_b128 v[184:187], v153 offset:32768
	ds_read_b128 v[188:191], v153 offset:33792
	ds_read_b128 v[192:195], v153 offset:34816
	ds_read_b128 v[196:199], v153 offset:35840
	ds_read_b128 v[200:203], v153 offset:36864
	ds_read_b128 v[204:207], v153 offset:37888
	ds_read_b128 v[208:211], v153 offset:38912
	ds_read_b128 v[212:215], v153 offset:39936
	global_load_lds_dwordx4 v[224:225], off
	v_lshl_add_u64 v[224:225], s[26:27], 0, v[134:135]
	s_mov_b32 m0, s68
	s_nop 0
	global_load_lds_dwordx4 v[224:225], off
	s_waitcnt vmcnt(8)
	s_waitcnt lgkmcnt(0)
	s_barrier
	v_mfma_f32_16x16x32_bf16 v[126:129], v[144:147], v[184:187], v[126:129]
	v_mfma_f32_16x16x32_bf16 v[118:121], v[160:163], v[184:187], v[118:121]
	v_mfma_f32_16x16x32_bf16 v[110:113], v[144:147], v[192:195], v[110:113]
	v_mfma_f32_16x16x32_bf16 v[102:105], v[160:163], v[192:195], v[102:105]
	v_mfma_f32_16x16x32_bf16 v[94:97], v[144:147], v[200:203], v[94:97]
	v_mfma_f32_16x16x32_bf16 v[86:89], v[160:163], v[200:203], v[86:89]
	v_mfma_f32_16x16x32_bf16 v[78:81], v[144:147], v[208:211], v[78:81]
	v_mfma_f32_16x16x32_bf16 v[70:73], v[160:163], v[208:211], v[70:73]
	v_mfma_f32_16x16x32_bf16 v[126:129], v[156:159], v[188:191], v[126:129]
	v_mfma_f32_16x16x32_bf16 v[118:121], v[164:167], v[188:191], v[118:121]
	v_mfma_f32_16x16x32_bf16 v[110:113], v[156:159], v[196:199], v[110:113]
	v_mfma_f32_16x16x32_bf16 v[102:105], v[164:167], v[196:199], v[102:105]
	v_mfma_f32_16x16x32_bf16 v[94:97], v[156:159], v[204:207], v[94:97]
	v_mfma_f32_16x16x32_bf16 v[86:89], v[164:167], v[204:207], v[86:89]
	v_mfma_f32_16x16x32_bf16 v[78:81], v[156:159], v[212:215], v[78:81]
	v_mfma_f32_16x16x32_bf16 v[70:73], v[164:167], v[212:215], v[70:73]
	v_mfma_f32_16x16x32_bf16 v[122:125], v[168:171], v[184:187], v[122:125]
	v_mfma_f32_16x16x32_bf16 v[114:117], v[176:179], v[184:187], v[114:117]
	v_mfma_f32_16x16x32_bf16 v[106:109], v[168:171], v[192:195], v[106:109]
	v_mfma_f32_16x16x32_bf16 v[98:101], v[176:179], v[192:195], v[98:101]
	v_mfma_f32_16x16x32_bf16 v[90:93], v[168:171], v[200:203], v[90:93]
	v_mfma_f32_16x16x32_bf16 v[82:85], v[176:179], v[200:203], v[82:85]
	v_mfma_f32_16x16x32_bf16 v[74:77], v[168:171], v[208:211], v[74:77]
	v_mfma_f32_16x16x32_bf16 v[66:69], v[176:179], v[208:211], v[66:69]
	v_mfma_f32_16x16x32_bf16 v[122:125], v[172:175], v[188:191], v[122:125]
	v_mfma_f32_16x16x32_bf16 v[114:117], v[180:183], v[188:191], v[114:117]
	v_mfma_f32_16x16x32_bf16 v[106:109], v[172:175], v[196:199], v[106:109]
	v_mfma_f32_16x16x32_bf16 v[98:101], v[180:183], v[196:199], v[98:101]
	v_mfma_f32_16x16x32_bf16 v[90:93], v[172:175], v[204:207], v[90:93]
	v_mfma_f32_16x16x32_bf16 v[82:85], v[180:183], v[204:207], v[82:85]
	v_mfma_f32_16x16x32_bf16 v[74:77], v[172:175], v[212:215], v[74:77]
	v_mfma_f32_16x16x32_bf16 v[66:69], v[180:183], v[212:215], v[66:69]
	s_barrier
	s_add_i32 s26, s86, s35
	v_lshl_add_u64 v[224:225], v[216:217], 0, s[16:17]
	s_mov_b32 m0, s26
	ds_read_b128 v[184:187], v153 offset:49152
	ds_read_b128 v[188:191], v153 offset:50176
	ds_read_b128 v[192:195], v153 offset:51200
	ds_read_b128 v[196:199], v153 offset:52224
	ds_read_b128 v[200:203], v153 offset:53248
	ds_read_b128 v[204:207], v153 offset:54272
	ds_read_b128 v[208:211], v153 offset:55296
	ds_read_b128 v[212:215], v153 offset:56320
	global_load_lds_dwordx4 v[224:225], off
	v_lshl_add_u64 v[224:225], v[216:217], 0, s[18:19]
	s_add_i32 m0, s26, 0x2000
	s_add_i32 s26, s87, s35
	global_load_lds_dwordx4 v[224:225], off
	v_lshl_add_u64 v[224:225], v[216:217], 0, s[22:23]
	s_mov_b32 m0, s26
	v_lshl_add_u64 v[216:217], v[216:217], 0, s[24:25]
	global_load_lds_dwordx4 v[224:225], off
	s_add_i32 m0, s26, 0x2000
	s_nop 0
	global_load_lds_dwordx4 v[216:217], off
	v_lshl_add_u64 v[216:217], v[220:221], 0, s[20:21]
	s_mov_b32 m0, s70
	s_nop 0
	global_load_lds_dwordx4 v[216:217], off
	v_lshl_add_u64 v[216:217], v[222:223], 0, s[20:21]
	s_mov_b32 m0, s71
	s_nop 0
	global_load_lds_dwordx4 v[216:217], off
	s_waitcnt vmcnt(8)
	s_waitcnt lgkmcnt(0)
	s_barrier
	v_mfma_f32_16x16x32_bf16 v[62:65], v[144:147], v[184:187], v[62:65]
	v_mfma_f32_16x16x32_bf16 v[54:57], v[160:163], v[184:187], v[54:57]
	v_mfma_f32_16x16x32_bf16 v[46:49], v[144:147], v[192:195], v[46:49]
	v_mfma_f32_16x16x32_bf16 v[38:41], v[160:163], v[192:195], v[38:41]
	v_mfma_f32_16x16x32_bf16 v[30:33], v[144:147], v[200:203], v[30:33]
	v_mfma_f32_16x16x32_bf16 v[22:25], v[160:163], v[200:203], v[22:25]
	v_mfma_f32_16x16x32_bf16 v[14:17], v[144:147], v[208:211], v[14:17]
	v_mfma_f32_16x16x32_bf16 v[6:9], v[160:163], v[208:211], v[6:9]
	v_mfma_f32_16x16x32_bf16 v[62:65], v[156:159], v[188:191], v[62:65]
	v_mfma_f32_16x16x32_bf16 v[54:57], v[164:167], v[188:191], v[54:57]
	v_mfma_f32_16x16x32_bf16 v[46:49], v[156:159], v[196:199], v[46:49]
	v_mfma_f32_16x16x32_bf16 v[38:41], v[164:167], v[196:199], v[38:41]
	v_mfma_f32_16x16x32_bf16 v[30:33], v[156:159], v[204:207], v[30:33]
	v_mfma_f32_16x16x32_bf16 v[22:25], v[164:167], v[204:207], v[22:25]
	v_mfma_f32_16x16x32_bf16 v[14:17], v[156:159], v[212:215], v[14:17]
	v_mfma_f32_16x16x32_bf16 v[6:9], v[164:167], v[212:215], v[6:9]
	v_mfma_f32_16x16x32_bf16 v[58:61], v[168:171], v[184:187], v[58:61]
	v_mfma_f32_16x16x32_bf16 v[50:53], v[176:179], v[184:187], v[50:53]
	v_mfma_f32_16x16x32_bf16 v[42:45], v[168:171], v[192:195], v[42:45]
	v_mfma_f32_16x16x32_bf16 v[34:37], v[176:179], v[192:195], v[34:37]
	v_mfma_f32_16x16x32_bf16 v[26:29], v[168:171], v[200:203], v[26:29]
	v_mfma_f32_16x16x32_bf16 v[18:21], v[176:179], v[200:203], v[18:21]
	v_mfma_f32_16x16x32_bf16 v[10:13], v[168:171], v[208:211], v[10:13]
	v_mfma_f32_16x16x32_bf16 v[2:5], v[176:179], v[208:211], v[2:5]
	v_mfma_f32_16x16x32_bf16 v[58:61], v[172:175], v[188:191], v[58:61]
	v_mfma_f32_16x16x32_bf16 v[50:53], v[180:183], v[188:191], v[50:53]
	v_mfma_f32_16x16x32_bf16 v[42:45], v[172:175], v[196:199], v[42:45]
	v_mfma_f32_16x16x32_bf16 v[34:37], v[180:183], v[196:199], v[34:37]
	v_mfma_f32_16x16x32_bf16 v[26:29], v[172:175], v[204:207], v[26:29]
	v_mfma_f32_16x16x32_bf16 v[18:21], v[180:183], v[204:207], v[18:21]
	v_mfma_f32_16x16x32_bf16 v[10:13], v[172:175], v[212:215], v[10:13]
	v_mfma_f32_16x16x32_bf16 v[2:5], v[180:183], v[212:215], v[2:5]
	s_barrier
	s_add_i32 s85, s85, 2
	s_add_u32 s83, s83, 0x10000
	s_addc_u32 s84, s84, 0
	s_add_u32 s62, s62, 0x100
	s_addc_u32 s63, s63, 0
	s_cmp_gt_u32 s85, 29

.LBB0_857:
	s_add_u32 s72, s50, 0x10000
	s_addc_u32 s73, s51, 0
	s_add_u32 s50, s52, 0xb0080
	s_addc_u32 s51, s53, 0
	s_mov_b32 s74, -2
	ds_read_b128 v[26:29], v185
	ds_read_b128 v[30:33], v185 offset:1024
	ds_read_b128 v[18:21], v185 offset:2048
	ds_read_b128 v[22:25], v185 offset:3072
	ds_read_b128 v[10:13], v186
	ds_read_b128 v[14:17], v186 offset:1024
	ds_read_b128 v[2:5], v186 offset:2048
	ds_read_b128 v[6:9], v186 offset:3072
	s_add_u32 s26, s50, 0xfff50080
	s_addc_u32 s27, s51, -1
	s_cmp_eq_u32 s74, 40
	s_cselect_b32 s53, s5, s27
	s_cselect_b32 s52, s4, s26
	s_cselect_b32 s55, s45, s73
	s_cselect_b32 s54, s44, s72
	v_lshl_add_u64 v[176:177], s[50:51], 0, v[168:169]
	s_add_i32 m0, s59, 0xc000
	ds_read_b128 v[190:193], v187
	ds_read_b128 v[194:197], v187 offset:1024
	ds_read_b128 v[198:201], v187 offset:2048
	ds_read_b128 v[202:205], v187 offset:3072
	ds_read_b128 v[206:209], v187 offset:4096
	ds_read_b128 v[210:213], v187 offset:5120
	ds_read_b128 v[220:223], v187 offset:6144
	ds_read_b128 v[224:227], v187 offset:7168
	global_load_lds_dwordx4 v[176:177], off
	v_lshl_add_u64 v[176:177], s[50:51], 0, v[170:171]
	s_add_i32 m0, s59, 0xe000
	s_nop 0
	global_load_lds_dwordx4 v[176:177], off
	s_waitcnt vmcnt(8)
	s_waitcnt lgkmcnt(0)
	s_barrier
	v_mfma_scale_f32_16x16x128_f8f6f4 v[158:161], v[26:33], v[190:197], 0, v188, v189 op_sel_hi:[0,0,0]
	v_mfma_scale_f32_16x16x128_f8f6f4 v[154:157], v[18:25], v[190:197], 0, v188, v189 op_sel_hi:[0,0,0]
	v_mfma_scale_f32_16x16x128_f8f6f4 v[150:153], v[26:33], v[198:205], 0, v188, v189 op_sel_hi:[0,0,0]
	v_mfma_scale_f32_16x16x128_f8f6f4 v[146:149], v[18:25], v[198:205], 0, v188, v189 op_sel_hi:[0,0,0]
	v_mfma_scale_f32_16x16x128_f8f6f4 v[138:141], v[26:33], v[206:213], 0, v188, v189 op_sel_hi:[0,0,0]
	v_mfma_scale_f32_16x16x128_f8f6f4 v[130:133], v[18:25], v[206:213], 0, v188, v189 op_sel_hi:[0,0,0]
	v_mfma_scale_f32_16x16x128_f8f6f4 v[122:125], v[26:33], v[220:227], 0, v188, v189 op_sel_hi:[0,0,0]
	v_mfma_scale_f32_16x16x128_f8f6f4 v[114:117], v[18:25], v[220:227], 0, v188, v189 op_sel_hi:[0,0,0]
	v_mfma_scale_f32_16x16x128_f8f6f4 v[142:145], v[10:17], v[190:197], 0, v188, v189 op_sel_hi:[0,0,0]
	v_mfma_scale_f32_16x16x128_f8f6f4 v[134:137], v[2:9], v[190:197], 0, v188, v189 op_sel_hi:[0,0,0]
	v_mfma_scale_f32_16x16x128_f8f6f4 v[126:129], v[10:17], v[198:205], 0, v188, v189 op_sel_hi:[0,0,0]
	v_mfma_scale_f32_16x16x128_f8f6f4 v[118:121], v[2:9], v[198:205], 0, v188, v189 op_sel_hi:[0,0,0]
	v_mfma_scale_f32_16x16x128_f8f6f4 v[110:113], v[10:17], v[206:213], 0, v188, v189 op_sel_hi:[0,0,0]
	v_mfma_scale_f32_16x16x128_f8f6f4 v[106:109], v[2:9], v[206:213], 0, v188, v189 op_sel_hi:[0,0,0]
	v_mfma_scale_f32_16x16x128_f8f6f4 v[102:105], v[10:17], v[220:227], 0, v188, v189 op_sel_hi:[0,0,0]
	v_mfma_scale_f32_16x16x128_f8f6f4 v[98:101], v[2:9], v[220:227], 0, v188, v189 op_sel_hi:[0,0,0]
	s_barrier
	s_add_i32 s26, s67, s57
	v_lshl_add_u64 v[176:177], s[54:55], 0, v[162:163]
	s_mov_b32 m0, s26
	ds_read_b128 v[190:193], v187 offset:16384
	ds_read_b128 v[194:197], v187 offset:17408
	ds_read_b128 v[198:201], v187 offset:18432
	ds_read_b128 v[202:205], v187 offset:19456
	ds_read_b128 v[206:209], v187 offset:20480
	ds_read_b128 v[210:213], v187 offset:21504
	ds_read_b128 v[220:223], v187 offset:22528
	ds_read_b128 v[224:227], v187 offset:23552
	global_load_lds_dwordx4 v[176:177], off
	v_lshl_add_u64 v[178:179], v[176:177], 0, s[8:9]
	s_add_i32 m0, s26, 0x2000
	s_add_i32 s26, s68, s57
	global_load_lds_dwordx4 v[178:179], off
	v_lshl_add_u64 v[178:179], v[176:177], 0, s[10:11]
	s_mov_b32 m0, s26
	v_lshl_add_u64 v[180:181], s[52:53], 0, v[166:167]
	global_load_lds_dwordx4 v[178:179], off
	v_lshl_add_u64 v[178:179], v[176:177], 0, s[12:13]
	s_add_i32 m0, s26, 0x2000
	s_nop 0
	global_load_lds_dwordx4 v[178:179], off
	v_lshl_add_u64 v[178:179], s[52:53], 0, v[164:165]
	s_mov_b32 m0, s59
	s_nop 0
	global_load_lds_dwordx4 v[178:179], off
	s_mov_b32 m0, s60
	s_nop 0
	global_load_lds_dwordx4 v[180:181], off
	s_waitcnt vmcnt(8)
	s_waitcnt lgkmcnt(0)
	s_barrier
	v_mfma_scale_f32_16x16x128_f8f6f4 v[94:97], v[26:33], v[190:197], 0, v188, v189 op_sel_hi:[0,0,0]
	v_mfma_scale_f32_16x16x128_f8f6f4 v[90:93], v[18:25], v[190:197], 0, v188, v189 op_sel_hi:[0,0,0]
	v_mfma_scale_f32_16x16x128_f8f6f4 v[86:89], v[26:33], v[198:205], 0, v188, v189 op_sel_hi:[0,0,0]
	v_mfma_scale_f32_16x16x128_f8f6f4 v[78:81], v[18:25], v[198:205], 0, v188, v189 op_sel_hi:[0,0,0]
	v_mfma_scale_f32_16x16x128_f8f6f4 v[70:73], v[26:33], v[206:213], 0, v188, v189 op_sel_hi:[0,0,0]
	v_mfma_scale_f32_16x16x128_f8f6f4 v[62:65], v[18:25], v[206:213], 0, v188, v189 op_sel_hi:[0,0,0]
	v_mfma_scale_f32_16x16x128_f8f6f4 v[54:57], v[26:33], v[220:227], 0, v188, v189 op_sel_hi:[0,0,0]
	v_mfma_scale_f32_16x16x128_f8f6f4 v[46:49], v[18:25], v[220:227], 0, v188, v189 op_sel_hi:[0,0,0]
	v_mfma_scale_f32_16x16x128_f8f6f4 v[82:85], v[10:17], v[190:197], 0, v188, v189 op_sel_hi:[0,0,0]
	v_mfma_scale_f32_16x16x128_f8f6f4 v[74:77], v[2:9], v[190:197], 0, v188, v189 op_sel_hi:[0,0,0]
	v_mfma_scale_f32_16x16x128_f8f6f4 v[66:69], v[10:17], v[198:205], 0, v188, v189 op_sel_hi:[0,0,0]
	v_mfma_scale_f32_16x16x128_f8f6f4 v[58:61], v[2:9], v[198:205], 0, v188, v189 op_sel_hi:[0,0,0]
	v_mfma_scale_f32_16x16x128_f8f6f4 v[50:53], v[10:17], v[206:213], 0, v188, v189 op_sel_hi:[0,0,0]
	v_mfma_scale_f32_16x16x128_f8f6f4 v[42:45], v[2:9], v[206:213], 0, v188, v189 op_sel_hi:[0,0,0]
	v_mfma_scale_f32_16x16x128_f8f6f4 v[38:41], v[10:17], v[220:227], 0, v188, v189 op_sel_hi:[0,0,0]
	v_mfma_scale_f32_16x16x128_f8f6f4 v[34:37], v[2:9], v[220:227], 0, v188, v189 op_sel_hi:[0,0,0]
	s_barrier
	s_add_i32 s54, 0, 0x18000
	s_add_i32 s55, 0, 0x1c000
	v_add_u32_e32 v14, s54, v183
	v_add_u32_e32 v30, s55, v183
	ds_read_b128 v[2:5], v14
	ds_read_b128 v[6:9], v14 offset:1024
	ds_read_b128 v[10:13], v14 offset:2048
	ds_read_b128 v[14:17], v14 offset:3072
	ds_read_b128 v[18:21], v30
	ds_read_b128 v[22:25], v30 offset:1024
	ds_read_b128 v[26:29], v30 offset:2048
	ds_read_b128 v[30:33], v30 offset:3072
	s_add_u32 s26, s52, 0xb0000
	s_addc_u32 s27, s53, 0
	s_mov_b32 m0, s61
	v_lshl_add_u64 v[214:215], s[26:27], 0, v[164:165]
	ds_read_b128 v[190:193], v187 offset:32768
	ds_read_b128 v[194:197], v187 offset:33792
	ds_read_b128 v[198:201], v187 offset:34816
	ds_read_b128 v[202:205], v187 offset:35840
	ds_read_b128 v[206:209], v187 offset:36864
	ds_read_b128 v[210:213], v187 offset:37888
	ds_read_b128 v[220:223], v187 offset:38912
	ds_read_b128 v[224:227], v187 offset:39936
	global_load_lds_dwordx4 v[214:215], off
	v_lshl_add_u64 v[214:215], s[26:27], 0, v[166:167]
	s_mov_b32 m0, s62
	s_nop 0
	global_load_lds_dwordx4 v[214:215], off
	s_waitcnt vmcnt(8)
	s_waitcnt lgkmcnt(0)
	s_barrier
	v_mfma_scale_f32_16x16x128_f8f6f4 v[158:161], v[2:9], v[190:197], v[158:161], v188, v189 op_sel_hi:[0,0,0]
	v_mfma_scale_f32_16x16x128_f8f6f4 v[154:157], v[10:17], v[190:197], v[154:157], v188, v189 op_sel_hi:[0,0,0]
	v_mfma_scale_f32_16x16x128_f8f6f4 v[150:153], v[2:9], v[198:205], v[150:153], v188, v189 op_sel_hi:[0,0,0]
	v_mfma_scale_f32_16x16x128_f8f6f4 v[146:149], v[10:17], v[198:205], v[146:149], v188, v189 op_sel_hi:[0,0,0]
	v_mfma_scale_f32_16x16x128_f8f6f4 v[138:141], v[2:9], v[206:213], v[138:141], v188, v189 op_sel_hi:[0,0,0]
	v_mfma_scale_f32_16x16x128_f8f6f4 v[130:133], v[10:17], v[206:213], v[130:133], v188, v189 op_sel_hi:[0,0,0]
	v_mfma_scale_f32_16x16x128_f8f6f4 v[122:125], v[2:9], v[220:227], v[122:125], v188, v189 op_sel_hi:[0,0,0]
	v_mfma_scale_f32_16x16x128_f8f6f4 v[114:117], v[10:17], v[220:227], v[114:117], v188, v189 op_sel_hi:[0,0,0]
	v_mfma_scale_f32_16x16x128_f8f6f4 v[142:145], v[18:25], v[190:197], v[142:145], v188, v189 op_sel_hi:[0,0,0]
	v_mfma_scale_f32_16x16x128_f8f6f4 v[134:137], v[26:33], v[190:197], v[134:137], v188, v189 op_sel_hi:[0,0,0]
	v_mfma_scale_f32_16x16x128_f8f6f4 v[126:129], v[18:25], v[198:205], v[126:129], v188, v189 op_sel_hi:[0,0,0]
	v_mfma_scale_f32_16x16x128_f8f6f4 v[118:121], v[26:33], v[198:205], v[118:121], v188, v189 op_sel_hi:[0,0,0]
	v_mfma_scale_f32_16x16x128_f8f6f4 v[110:113], v[18:25], v[206:213], v[110:113], v188, v189 op_sel_hi:[0,0,0]
	v_mfma_scale_f32_16x16x128_f8f6f4 v[106:109], v[26:33], v[206:213], v[106:109], v188, v189 op_sel_hi:[0,0,0]
	v_mfma_scale_f32_16x16x128_f8f6f4 v[102:105], v[18:25], v[220:227], v[102:105], v188, v189 op_sel_hi:[0,0,0]
	v_mfma_scale_f32_16x16x128_f8f6f4 v[98:101], v[26:33], v[220:227], v[98:101], v188, v189 op_sel_hi:[0,0,0]
	s_barrier
	s_add_i32 s26, s54, s57
	v_lshl_add_u64 v[214:215], v[176:177], 0, s[16:17]
	s_mov_b32 m0, s26
	ds_read_b128 v[190:193], v187 offset:49152
	ds_read_b128 v[194:197], v187 offset:50176
	ds_read_b128 v[198:201], v187 offset:51200
	ds_read_b128 v[202:205], v187 offset:52224
	ds_read_b128 v[206:209], v187 offset:53248
	ds_read_b128 v[210:213], v187 offset:54272
	ds_read_b128 v[220:223], v187 offset:55296
	ds_read_b128 v[224:227], v187 offset:56320
	global_load_lds_dwordx4 v[214:215], off
	v_lshl_add_u64 v[214:215], v[176:177], 0, s[18:19]
	s_add_i32 m0, s26, 0x2000
	s_add_i32 s26, s55, s57
	global_load_lds_dwordx4 v[214:215], off
	v_lshl_add_u64 v[214:215], v[176:177], 0, s[22:23]
	s_mov_b32 m0, s26
	v_lshl_add_u64 v[176:177], v[176:177], 0, s[24:25]
	global_load_lds_dwordx4 v[214:215], off
	s_add_i32 m0, s26, 0x2000
	s_nop 0
	global_load_lds_dwordx4 v[176:177], off
	v_lshl_add_u64 v[176:177], v[178:179], 0, s[20:21]
	s_mov_b32 m0, s64
	s_nop 0
	global_load_lds_dwordx4 v[176:177], off
	v_lshl_add_u64 v[176:177], v[180:181], 0, s[20:21]
	s_mov_b32 m0, s65
	s_nop 0
	global_load_lds_dwordx4 v[176:177], off
	s_waitcnt vmcnt(8)
	s_waitcnt lgkmcnt(0)
	s_barrier
	v_mfma_scale_f32_16x16x128_f8f6f4 v[94:97], v[2:9], v[190:197], v[94:97], v188, v189 op_sel_hi:[0,0,0]
	v_mfma_scale_f32_16x16x128_f8f6f4 v[90:93], v[10:17], v[190:197], v[90:93], v188, v189 op_sel_hi:[0,0,0]
	v_mfma_scale_f32_16x16x128_f8f6f4 v[86:89], v[2:9], v[198:205], v[86:89], v188, v189 op_sel_hi:[0,0,0]
	v_mfma_scale_f32_16x16x128_f8f6f4 v[78:81], v[10:17], v[198:205], v[78:81], v188, v189 op_sel_hi:[0,0,0]
	v_mfma_scale_f32_16x16x128_f8f6f4 v[70:73], v[2:9], v[206:213], v[70:73], v188, v189 op_sel_hi:[0,0,0]
	v_mfma_scale_f32_16x16x128_f8f6f4 v[62:65], v[10:17], v[206:213], v[62:65], v188, v189 op_sel_hi:[0,0,0]
	v_mfma_scale_f32_16x16x128_f8f6f4 v[54:57], v[2:9], v[220:227], v[54:57], v188, v189 op_sel_hi:[0,0,0]
	v_mfma_scale_f32_16x16x128_f8f6f4 v[46:49], v[10:17], v[220:227], v[46:49], v188, v189 op_sel_hi:[0,0,0]
	v_mfma_scale_f32_16x16x128_f8f6f4 v[82:85], v[18:25], v[190:197], v[82:85], v188, v189 op_sel_hi:[0,0,0]
	v_mfma_scale_f32_16x16x128_f8f6f4 v[74:77], v[26:33], v[190:197], v[74:77], v188, v189 op_sel_hi:[0,0,0]
	v_mfma_scale_f32_16x16x128_f8f6f4 v[66:69], v[18:25], v[198:205], v[66:69], v188, v189 op_sel_hi:[0,0,0]
	v_mfma_scale_f32_16x16x128_f8f6f4 v[58:61], v[26:33], v[198:205], v[58:61], v188, v189 op_sel_hi:[0,0,0]
	v_mfma_scale_f32_16x16x128_f8f6f4 v[50:53], v[18:25], v[206:213], v[50:53], v188, v189 op_sel_hi:[0,0,0]
	v_mfma_scale_f32_16x16x128_f8f6f4 v[42:45], v[26:33], v[206:213], v[42:45], v188, v189 op_sel_hi:[0,0,0]
	v_mfma_scale_f32_16x16x128_f8f6f4 v[38:41], v[18:25], v[220:227], v[38:41], v188, v189 op_sel_hi:[0,0,0]
	v_mfma_scale_f32_16x16x128_f8f6f4 v[34:37], v[26:33], v[220:227], v[34:37], v188, v189 op_sel_hi:[0,0,0]
	s_barrier
	s_add_i32 s74, s74, 2
	s_add_u32 s72, s72, 0x10000
	s_addc_u32 s73, s73, 0
	s_add_u32 s50, s50, 0x100
	s_addc_u32 s51, s51, 0
	s_cmp_gt_u32 s74, 41

.LBB0_984:
	s_ashr_i32 s45, s44, 31
	s_lshl_b64 s[26:27], s[44:45], 19
	v_readlane_b32 s50, v254, 56
	v_readlane_b32 s51, v254, 57
	s_add_u32 s50, s50, s26
	s_addc_u32 s51, s51, s27
	s_and_b64 s[26:27], s[0:1], exec
	s_cselect_b32 s45, s51, s59
	s_cselect_b32 s72, s50, s58
	s_ashr_i32 s41, s40, 31
	s_lshl_b64 s[26:27], s[40:41], 19
	s_add_u32 s52, s3, s26
	s_addc_u32 s53, s33, s27
	s_and_b64 s[26:27], s[0:1], exec
	s_cselect_b32 s41, s53, s57
	s_cselect_b32 s73, s52, s56
	s_add_u32 s74, s56, 0x10000
	s_addc_u32 s75, s57, 0
	s_add_u32 s56, s58, 0x40080
	s_addc_u32 s57, s59, 0
	s_mov_b32 s80, -2
	ds_read_b128 v[26:29], v185
	ds_read_b128 v[30:33], v185 offset:1024
	ds_read_b128 v[18:21], v185 offset:2048
	ds_read_b128 v[22:25], v185 offset:3072
	ds_read_b128 v[10:13], v186
	ds_read_b128 v[14:17], v186 offset:1024
	ds_read_b128 v[2:5], v186 offset:2048
	ds_read_b128 v[6:9], v186 offset:3072
	s_add_u32 s26, s56, 0xfffc0080
	s_addc_u32 s27, s57, -1
	s_cmp_eq_u32 s80, 12
	s_cselect_b32 s59, s45, s27
	s_cselect_b32 s58, s72, s26
	s_cselect_b32 s61, s41, s75
	s_cselect_b32 s60, s73, s74
	v_lshl_add_u64 v[176:177], s[56:57], 0, v[168:169]
	s_add_i32 m0, s55, 0xc000
	ds_read_b128 v[192:195], v187
	ds_read_b128 v[196:199], v187 offset:1024
	ds_read_b128 v[200:203], v187 offset:2048
	ds_read_b128 v[204:207], v187 offset:3072
	ds_read_b128 v[208:211], v187 offset:4096
	ds_read_b128 v[212:215], v187 offset:5120
	ds_read_b128 v[220:223], v187 offset:6144
	ds_read_b128 v[224:227], v187 offset:7168
	global_load_lds_dwordx4 v[176:177], off
	v_lshl_add_u64 v[176:177], s[56:57], 0, v[170:171]
	s_add_i32 m0, s55, 0xe000
	s_nop 0
	global_load_lds_dwordx4 v[176:177], off
	s_waitcnt vmcnt(24)
	s_waitcnt lgkmcnt(0)
	s_barrier
	v_mfma_scale_f32_16x16x128_f8f6f4 v[158:161], v[26:33], v[192:199], 0, v188, v189 op_sel_hi:[0,0,0]
	v_mfma_scale_f32_16x16x128_f8f6f4 v[154:157], v[18:25], v[192:199], 0, v188, v189 op_sel_hi:[0,0,0]
	v_mfma_scale_f32_16x16x128_f8f6f4 v[146:149], v[26:33], v[200:207], 0, v188, v189 op_sel_hi:[0,0,0]
	v_mfma_scale_f32_16x16x128_f8f6f4 v[138:141], v[18:25], v[200:207], 0, v188, v189 op_sel_hi:[0,0,0]
	v_mfma_scale_f32_16x16x128_f8f6f4 v[130:133], v[26:33], v[208:215], 0, v188, v189 op_sel_hi:[0,0,0]
	v_mfma_scale_f32_16x16x128_f8f6f4 v[122:125], v[18:25], v[208:215], 0, v188, v189 op_sel_hi:[0,0,0]
	v_mfma_scale_f32_16x16x128_f8f6f4 v[114:117], v[26:33], v[220:227], 0, v188, v189 op_sel_hi:[0,0,0]
	v_mfma_scale_f32_16x16x128_f8f6f4 v[106:109], v[18:25], v[220:227], 0, v188, v189 op_sel_hi:[0,0,0]
	v_mfma_scale_f32_16x16x128_f8f6f4 v[150:153], v[10:17], v[192:199], 0, v188, v189 op_sel_hi:[0,0,0]
	v_mfma_scale_f32_16x16x128_f8f6f4 v[142:145], v[2:9], v[192:199], 0, v188, v189 op_sel_hi:[0,0,0]
	v_mfma_scale_f32_16x16x128_f8f6f4 v[134:137], v[10:17], v[200:207], 0, v188, v189 op_sel_hi:[0,0,0]
	v_mfma_scale_f32_16x16x128_f8f6f4 v[126:129], v[2:9], v[200:207], 0, v188, v189 op_sel_hi:[0,0,0]
	v_mfma_scale_f32_16x16x128_f8f6f4 v[118:121], v[10:17], v[208:215], 0, v188, v189 op_sel_hi:[0,0,0]
	v_mfma_scale_f32_16x16x128_f8f6f4 v[110:113], v[2:9], v[208:215], 0, v188, v189 op_sel_hi:[0,0,0]
	v_mfma_scale_f32_16x16x128_f8f6f4 v[102:105], v[10:17], v[220:227], 0, v188, v189 op_sel_hi:[0,0,0]
	v_mfma_scale_f32_16x16x128_f8f6f4 v[98:101], v[2:9], v[220:227], 0, v188, v189 op_sel_hi:[0,0,0]
	s_barrier
	s_add_i32 s26, s70, s35
	v_lshl_add_u64 v[176:177], s[60:61], 0, v[162:163]
	s_mov_b32 m0, s26
	ds_read_b128 v[192:195], v187 offset:16384
	ds_read_b128 v[196:199], v187 offset:17408
	ds_read_b128 v[200:203], v187 offset:18432
	ds_read_b128 v[204:207], v187 offset:19456
	ds_read_b128 v[208:211], v187 offset:20480
	ds_read_b128 v[212:215], v187 offset:21504
	ds_read_b128 v[220:223], v187 offset:22528
	ds_read_b128 v[224:227], v187 offset:23552
	global_load_lds_dwordx4 v[176:177], off
	v_lshl_add_u64 v[178:179], v[176:177], 0, s[6:7]
	s_add_i32 m0, s26, 0x2000
	s_add_i32 s26, s71, s35
	global_load_lds_dwordx4 v[178:179], off
	v_lshl_add_u64 v[178:179], v[176:177], 0, s[8:9]
	s_mov_b32 m0, s26
	v_lshl_add_u64 v[180:181], s[58:59], 0, v[166:167]
	global_load_lds_dwordx4 v[178:179], off
	v_lshl_add_u64 v[178:179], v[176:177], 0, s[10:11]
	s_add_i32 m0, s26, 0x2000
	s_nop 0
	global_load_lds_dwordx4 v[178:179], off
	v_lshl_add_u64 v[178:179], s[58:59], 0, v[164:165]
	s_mov_b32 m0, s55
	s_nop 0
	global_load_lds_dwordx4 v[178:179], off
	s_mov_b32 m0, s63
	s_nop 0
	global_load_lds_dwordx4 v[180:181], off
	s_waitcnt vmcnt(24)
	s_waitcnt lgkmcnt(0)
	s_barrier
	v_mfma_scale_f32_16x16x128_f8f6f4 v[94:97], v[26:33], v[192:199], 0, v188, v189 op_sel_hi:[0,0,0]
	v_mfma_scale_f32_16x16x128_f8f6f4 v[90:93], v[18:25], v[192:199], 0, v188, v189 op_sel_hi:[0,0,0]
	v_mfma_scale_f32_16x16x128_f8f6f4 v[82:85], v[26:33], v[200:207], 0, v188, v189 op_sel_hi:[0,0,0]
	v_mfma_scale_f32_16x16x128_f8f6f4 v[74:77], v[18:25], v[200:207], 0, v188, v189 op_sel_hi:[0,0,0]
	v_mfma_scale_f32_16x16x128_f8f6f4 v[66:69], v[26:33], v[208:215], 0, v188, v189 op_sel_hi:[0,0,0]
	v_mfma_scale_f32_16x16x128_f8f6f4 v[58:61], v[18:25], v[208:215], 0, v188, v189 op_sel_hi:[0,0,0]
	v_mfma_scale_f32_16x16x128_f8f6f4 v[50:53], v[26:33], v[220:227], 0, v188, v189 op_sel_hi:[0,0,0]
	v_mfma_scale_f32_16x16x128_f8f6f4 v[42:45], v[18:25], v[220:227], 0, v188, v189 op_sel_hi:[0,0,0]
	v_mfma_scale_f32_16x16x128_f8f6f4 v[86:89], v[10:17], v[192:199], 0, v188, v189 op_sel_hi:[0,0,0]
	v_mfma_scale_f32_16x16x128_f8f6f4 v[78:81], v[2:9], v[192:199], 0, v188, v189 op_sel_hi:[0,0,0]
	v_mfma_scale_f32_16x16x128_f8f6f4 v[70:73], v[10:17], v[200:207], 0, v188, v189 op_sel_hi:[0,0,0]
	v_mfma_scale_f32_16x16x128_f8f6f4 v[62:65], v[2:9], v[200:207], 0, v188, v189 op_sel_hi:[0,0,0]
	v_mfma_scale_f32_16x16x128_f8f6f4 v[54:57], v[10:17], v[208:215], 0, v188, v189 op_sel_hi:[0,0,0]
	v_mfma_scale_f32_16x16x128_f8f6f4 v[46:49], v[2:9], v[208:215], 0, v188, v189 op_sel_hi:[0,0,0]
	v_mfma_scale_f32_16x16x128_f8f6f4 v[38:41], v[10:17], v[220:227], 0, v188, v189 op_sel_hi:[0,0,0]
	v_mfma_scale_f32_16x16x128_f8f6f4 v[34:37], v[2:9], v[220:227], 0, v188, v189 op_sel_hi:[0,0,0]
	s_barrier
	s_add_i32 s60, 0, 0x18000
	s_add_i32 s61, 0, 0x1c000
	v_add_u32_e32 v14, s60, v183
	v_add_u32_e32 v30, s61, v183
	ds_read_b128 v[2:5], v14
	ds_read_b128 v[6:9], v14 offset:1024
	ds_read_b128 v[10:13], v14 offset:2048
	ds_read_b128 v[14:17], v14 offset:3072
	ds_read_b128 v[18:21], v30
	ds_read_b128 v[22:25], v30 offset:1024
	ds_read_b128 v[26:29], v30 offset:2048
	ds_read_b128 v[30:33], v30 offset:3072
	s_add_u32 s26, s58, 0x40000
	s_addc_u32 s27, s59, 0
	s_mov_b32 m0, s64
	v_lshl_add_u64 v[216:217], s[26:27], 0, v[164:165]
	ds_read_b128 v[192:195], v187 offset:32768
	ds_read_b128 v[196:199], v187 offset:33792
	ds_read_b128 v[200:203], v187 offset:34816
	ds_read_b128 v[204:207], v187 offset:35840
	ds_read_b128 v[208:211], v187 offset:36864
	ds_read_b128 v[212:215], v187 offset:37888
	ds_read_b128 v[220:223], v187 offset:38912
	ds_read_b128 v[224:227], v187 offset:39936
	global_load_lds_dwordx4 v[216:217], off
	v_lshl_add_u64 v[216:217], s[26:27], 0, v[166:167]
	s_mov_b32 m0, s65
	s_nop 0
	global_load_lds_dwordx4 v[216:217], off
	s_waitcnt vmcnt(8)
	s_waitcnt lgkmcnt(0)
	s_barrier
	v_mfma_scale_f32_16x16x128_f8f6f4 v[158:161], v[2:9], v[192:199], v[158:161], v188, v189 op_sel_hi:[0,0,0]
	v_mfma_scale_f32_16x16x128_f8f6f4 v[154:157], v[10:17], v[192:199], v[154:157], v188, v189 op_sel_hi:[0,0,0]
	v_mfma_scale_f32_16x16x128_f8f6f4 v[146:149], v[2:9], v[200:207], v[146:149], v188, v189 op_sel_hi:[0,0,0]
	v_mfma_scale_f32_16x16x128_f8f6f4 v[138:141], v[10:17], v[200:207], v[138:141], v188, v189 op_sel_hi:[0,0,0]
	v_mfma_scale_f32_16x16x128_f8f6f4 v[130:133], v[2:9], v[208:215], v[130:133], v188, v189 op_sel_hi:[0,0,0]
	v_mfma_scale_f32_16x16x128_f8f6f4 v[122:125], v[10:17], v[208:215], v[122:125], v188, v189 op_sel_hi:[0,0,0]
	v_mfma_scale_f32_16x16x128_f8f6f4 v[114:117], v[2:9], v[220:227], v[114:117], v188, v189 op_sel_hi:[0,0,0]
	v_mfma_scale_f32_16x16x128_f8f6f4 v[106:109], v[10:17], v[220:227], v[106:109], v188, v189 op_sel_hi:[0,0,0]
	v_mfma_scale_f32_16x16x128_f8f6f4 v[150:153], v[18:25], v[192:199], v[150:153], v188, v189 op_sel_hi:[0,0,0]
	v_mfma_scale_f32_16x16x128_f8f6f4 v[142:145], v[26:33], v[192:199], v[142:145], v188, v189 op_sel_hi:[0,0,0]
	v_mfma_scale_f32_16x16x128_f8f6f4 v[134:137], v[18:25], v[200:207], v[134:137], v188, v189 op_sel_hi:[0,0,0]
	v_mfma_scale_f32_16x16x128_f8f6f4 v[126:129], v[26:33], v[200:207], v[126:129], v188, v189 op_sel_hi:[0,0,0]
	v_mfma_scale_f32_16x16x128_f8f6f4 v[118:121], v[18:25], v[208:215], v[118:121], v188, v189 op_sel_hi:[0,0,0]
	v_mfma_scale_f32_16x16x128_f8f6f4 v[110:113], v[26:33], v[208:215], v[110:113], v188, v189 op_sel_hi:[0,0,0]
	v_mfma_scale_f32_16x16x128_f8f6f4 v[102:105], v[18:25], v[220:227], v[102:105], v188, v189 op_sel_hi:[0,0,0]
	v_mfma_scale_f32_16x16x128_f8f6f4 v[98:101], v[26:33], v[220:227], v[98:101], v188, v189 op_sel_hi:[0,0,0]
	s_barrier
	s_add_i32 s26, s60, s35
	v_lshl_add_u64 v[216:217], v[176:177], 0, s[14:15]
	s_mov_b32 m0, s26
	ds_read_b128 v[192:195], v187 offset:49152
	ds_read_b128 v[196:199], v187 offset:50176
	ds_read_b128 v[200:203], v187 offset:51200
	ds_read_b128 v[204:207], v187 offset:52224
	ds_read_b128 v[208:211], v187 offset:53248
	ds_read_b128 v[212:215], v187 offset:54272
	ds_read_b128 v[220:223], v187 offset:55296
	ds_read_b128 v[224:227], v187 offset:56320
	global_load_lds_dwordx4 v[216:217], off
	v_lshl_add_u64 v[216:217], v[176:177], 0, s[16:17]
	s_add_i32 m0, s26, 0x2000
	s_add_i32 s26, s61, s35
	global_load_lds_dwordx4 v[216:217], off
	v_lshl_add_u64 v[216:217], v[176:177], 0, s[20:21]
	s_mov_b32 m0, s26
	v_lshl_add_u64 v[176:177], v[176:177], 0, s[22:23]
	global_load_lds_dwordx4 v[216:217], off
	s_add_i32 m0, s26, 0x2000
	s_nop 0
	global_load_lds_dwordx4 v[176:177], off
	v_lshl_add_u64 v[176:177], v[178:179], 0, s[18:19]
	s_mov_b32 m0, s67
	s_nop 0
	global_load_lds_dwordx4 v[176:177], off
	v_lshl_add_u64 v[176:177], v[180:181], 0, s[18:19]
	s_mov_b32 m0, s68
	s_nop 0
	global_load_lds_dwordx4 v[176:177], off
	s_waitcnt vmcnt(8)
	s_waitcnt lgkmcnt(0)
	s_barrier
	v_mfma_scale_f32_16x16x128_f8f6f4 v[94:97], v[2:9], v[192:199], v[94:97], v188, v189 op_sel_hi:[0,0,0]
	v_mfma_scale_f32_16x16x128_f8f6f4 v[90:93], v[10:17], v[192:199], v[90:93], v188, v189 op_sel_hi:[0,0,0]
	v_mfma_scale_f32_16x16x128_f8f6f4 v[82:85], v[2:9], v[200:207], v[82:85], v188, v189 op_sel_hi:[0,0,0]
	v_mfma_scale_f32_16x16x128_f8f6f4 v[74:77], v[10:17], v[200:207], v[74:77], v188, v189 op_sel_hi:[0,0,0]
	v_mfma_scale_f32_16x16x128_f8f6f4 v[66:69], v[2:9], v[208:215], v[66:69], v188, v189 op_sel_hi:[0,0,0]
	v_mfma_scale_f32_16x16x128_f8f6f4 v[58:61], v[10:17], v[208:215], v[58:61], v188, v189 op_sel_hi:[0,0,0]
	v_mfma_scale_f32_16x16x128_f8f6f4 v[50:53], v[2:9], v[220:227], v[50:53], v188, v189 op_sel_hi:[0,0,0]
	v_mfma_scale_f32_16x16x128_f8f6f4 v[42:45], v[10:17], v[220:227], v[42:45], v188, v189 op_sel_hi:[0,0,0]
	v_mfma_scale_f32_16x16x128_f8f6f4 v[86:89], v[18:25], v[192:199], v[86:89], v188, v189 op_sel_hi:[0,0,0]
	v_mfma_scale_f32_16x16x128_f8f6f4 v[78:81], v[26:33], v[192:199], v[78:81], v188, v189 op_sel_hi:[0,0,0]
	v_mfma_scale_f32_16x16x128_f8f6f4 v[70:73], v[18:25], v[200:207], v[70:73], v188, v189 op_sel_hi:[0,0,0]
	v_mfma_scale_f32_16x16x128_f8f6f4 v[62:65], v[26:33], v[200:207], v[62:65], v188, v189 op_sel_hi:[0,0,0]
	v_mfma_scale_f32_16x16x128_f8f6f4 v[54:57], v[18:25], v[208:215], v[54:57], v188, v189 op_sel_hi:[0,0,0]
	v_mfma_scale_f32_16x16x128_f8f6f4 v[46:49], v[26:33], v[208:215], v[46:49], v188, v189 op_sel_hi:[0,0,0]
	v_mfma_scale_f32_16x16x128_f8f6f4 v[38:41], v[18:25], v[220:227], v[38:41], v188, v189 op_sel_hi:[0,0,0]
	v_mfma_scale_f32_16x16x128_f8f6f4 v[34:37], v[26:33], v[220:227], v[34:37], v188, v189 op_sel_hi:[0,0,0]
	s_barrier
	s_add_i32 s80, s80, 2
	s_add_u32 s74, s74, 0x10000
	s_addc_u32 s75, s75, 0
	s_add_u32 s56, s56, 0x100
	s_addc_u32 s57, s57, 0
	s_cmp_gt_u32 s80, 13

.LBB0_1191:
	s_ashr_i32 s45, s44, 31
	s_lshl_b64 s[26:27], s[44:45], 19
	s_add_u32 s50, s4, s26
	s_addc_u32 s51, s5, s27
	s_and_b64 s[26:27], s[0:1], exec
	s_cselect_b32 s45, s51, s59
	s_cselect_b32 s69, s50, s58
	s_ashr_i32 s41, s40, 31
	s_lshl_b64 s[26:27], s[40:41], 19
	s_add_u32 s52, s3, s26
	s_addc_u32 s53, s33, s27
	s_and_b64 s[26:27], s[0:1], exec
	s_cselect_b32 s41, s53, s57
	s_cselect_b32 s70, s52, s56
	s_add_u32 s71, s56, 0x10000
	s_addc_u32 s72, s57, 0
	s_add_u32 s56, s58, 0x40080
	s_addc_u32 s57, s59, 0
	s_mov_b32 s73, -2
	ds_read_b128 v[66:69], v199
	ds_read_b128 v[70:73], v199 offset:1024
	ds_read_b128 v[82:85], v199 offset:2048
	ds_read_b128 v[86:89], v199 offset:3072
	ds_read_b128 v[146:149], v200
	ds_read_b128 v[150:153], v200 offset:1024
	ds_read_b128 v[154:157], v200 offset:2048
	ds_read_b128 v[158:161], v200 offset:3072
	s_add_u32 s26, s56, 0xfffc0080
	s_addc_u32 s27, s57, -1
	s_cmp_eq_u32 s73, 12
	s_cselect_b32 s59, s45, s27
	s_cselect_b32 s58, s69, s26
	s_cselect_b32 s27, s41, s72
	s_cselect_b32 s26, s70, s71
	v_lshl_add_u64 v[214:215], s[56:57], 0, v[176:177]
	s_add_i32 m0, s55, 0xc000
	ds_read_b128 v[162:165], v201
	ds_read_b128 v[166:169], v201 offset:1024
	ds_read_b128 v[184:187], v201 offset:2048
	ds_read_b128 v[188:191], v201 offset:3072
	ds_read_b128 v[192:195], v201 offset:4096
	ds_read_b128 v[202:205], v201 offset:5120
	ds_read_b128 v[206:209], v201 offset:6144
	ds_read_b128 v[210:213], v201 offset:7168
	global_load_lds_dwordx4 v[214:215], off
	v_lshl_add_u64 v[214:215], s[56:57], 0, v[178:179]
	s_add_i32 m0, s55, 0xe000
	s_nop 0
	global_load_lds_dwordx4 v[214:215], off
	s_waitcnt vmcnt(8)
	s_waitcnt lgkmcnt(0)
	s_barrier
	v_mfma_f32_16x16x32_bf16 v[142:145], v[66:69], v[162:165], 0
	v_mfma_f32_16x16x32_bf16 v[138:141], v[82:85], v[162:165], 0
	v_mfma_f32_16x16x32_bf16 v[126:129], v[66:69], v[184:187], 0
	v_mfma_f32_16x16x32_bf16 v[122:125], v[82:85], v[184:187], 0
	v_mfma_f32_16x16x32_bf16 v[110:113], v[66:69], v[192:195], 0
	v_mfma_f32_16x16x32_bf16 v[106:109], v[82:85], v[192:195], 0
	v_mfma_f32_16x16x32_bf16 v[94:97], v[66:69], v[206:209], 0
	v_mfma_f32_16x16x32_bf16 v[90:93], v[82:85], v[206:209], 0
	v_mfma_f32_16x16x32_bf16 v[142:145], v[70:73], v[166:169], v[142:145]
	v_mfma_f32_16x16x32_bf16 v[138:141], v[86:89], v[166:169], v[138:141]
	v_mfma_f32_16x16x32_bf16 v[126:129], v[70:73], v[188:191], v[126:129]
	v_mfma_f32_16x16x32_bf16 v[122:125], v[86:89], v[188:191], v[122:125]
	v_mfma_f32_16x16x32_bf16 v[110:113], v[70:73], v[202:205], v[110:113]
	v_mfma_f32_16x16x32_bf16 v[106:109], v[86:89], v[202:205], v[106:109]
	v_mfma_f32_16x16x32_bf16 v[94:97], v[70:73], v[210:213], v[94:97]
	v_mfma_f32_16x16x32_bf16 v[90:93], v[86:89], v[210:213], v[90:93]
	v_mfma_f32_16x16x32_bf16 v[134:137], v[146:149], v[162:165], 0
	v_mfma_f32_16x16x32_bf16 v[130:133], v[154:157], v[162:165], 0
	v_mfma_f32_16x16x32_bf16 v[118:121], v[146:149], v[184:187], 0
	v_mfma_f32_16x16x32_bf16 v[114:117], v[154:157], v[184:187], 0
	v_mfma_f32_16x16x32_bf16 v[102:105], v[146:149], v[192:195], 0
	v_mfma_f32_16x16x32_bf16 v[98:101], v[154:157], v[192:195], 0
	v_mfma_f32_16x16x32_bf16 v[78:81], v[146:149], v[206:209], 0
	v_mfma_f32_16x16x32_bf16 v[74:77], v[154:157], v[206:209], 0
	v_mfma_f32_16x16x32_bf16 v[134:137], v[150:153], v[166:169], v[134:137]
	v_mfma_f32_16x16x32_bf16 v[130:133], v[158:161], v[166:169], v[130:133]
	v_mfma_f32_16x16x32_bf16 v[118:121], v[150:153], v[188:191], v[118:121]
	v_mfma_f32_16x16x32_bf16 v[114:117], v[158:161], v[188:191], v[114:117]
	v_mfma_f32_16x16x32_bf16 v[102:105], v[150:153], v[202:205], v[102:105]
	v_mfma_f32_16x16x32_bf16 v[98:101], v[158:161], v[202:205], v[98:101]
	v_mfma_f32_16x16x32_bf16 v[78:81], v[150:153], v[210:213], v[78:81]
	v_mfma_f32_16x16x32_bf16 v[74:77], v[158:161], v[210:213], v[74:77]
	s_barrier
	v_lshl_add_u64 v[214:215], s[26:27], 0, v[170:171]
	s_add_i32 s26, s67, s35
	s_mov_b32 m0, s26
	ds_read_b128 v[162:165], v201 offset:16384
	ds_read_b128 v[166:169], v201 offset:17408
	ds_read_b128 v[184:187], v201 offset:18432
	ds_read_b128 v[188:191], v201 offset:19456
	ds_read_b128 v[192:195], v201 offset:20480
	ds_read_b128 v[202:205], v201 offset:21504
	ds_read_b128 v[206:209], v201 offset:22528
	ds_read_b128 v[210:213], v201 offset:23552
	global_load_lds_dwordx4 v[214:215], off
	v_lshl_add_u64 v[216:217], v[214:215], 0, s[6:7]
	s_add_i32 m0, s26, 0x2000
	s_add_i32 s26, s68, s35
	global_load_lds_dwordx4 v[216:217], off
	v_lshl_add_u64 v[216:217], v[214:215], 0, s[10:11]
	s_mov_b32 m0, s26
	v_lshl_add_u64 v[220:221], s[58:59], 0, v[174:175]
	global_load_lds_dwordx4 v[216:217], off
	v_lshl_add_u64 v[216:217], v[214:215], 0, s[12:13]
	s_add_i32 m0, s26, 0x2000
	s_nop 0
	global_load_lds_dwordx4 v[216:217], off
	v_lshl_add_u64 v[216:217], s[58:59], 0, v[172:173]
	s_mov_b32 m0, s55
	s_nop 0
	global_load_lds_dwordx4 v[216:217], off
	s_mov_b32 m0, s60
	s_nop 0
	global_load_lds_dwordx4 v[220:221], off
	s_waitcnt vmcnt(8)
	s_waitcnt lgkmcnt(0)
	s_barrier
	v_mfma_f32_16x16x32_bf16 v[62:65], v[66:69], v[162:165], 0
	v_mfma_f32_16x16x32_bf16 v[58:61], v[82:85], v[162:165], 0
	v_mfma_f32_16x16x32_bf16 v[46:49], v[66:69], v[184:187], 0
	v_mfma_f32_16x16x32_bf16 v[42:45], v[82:85], v[184:187], 0
	v_mfma_f32_16x16x32_bf16 v[30:33], v[66:69], v[192:195], 0
	v_mfma_f32_16x16x32_bf16 v[26:29], v[82:85], v[192:195], 0
	v_mfma_f32_16x16x32_bf16 v[14:17], v[66:69], v[206:209], 0
	v_mfma_f32_16x16x32_bf16 v[10:13], v[82:85], v[206:209], 0
	v_mfma_f32_16x16x32_bf16 v[62:65], v[70:73], v[166:169], v[62:65]
	v_mfma_f32_16x16x32_bf16 v[58:61], v[86:89], v[166:169], v[58:61]
	v_mfma_f32_16x16x32_bf16 v[46:49], v[70:73], v[188:191], v[46:49]
	v_mfma_f32_16x16x32_bf16 v[42:45], v[86:89], v[188:191], v[42:45]
	v_mfma_f32_16x16x32_bf16 v[30:33], v[70:73], v[202:205], v[30:33]
	v_mfma_f32_16x16x32_bf16 v[26:29], v[86:89], v[202:205], v[26:29]
	v_mfma_f32_16x16x32_bf16 v[14:17], v[70:73], v[210:213], v[14:17]
	v_mfma_f32_16x16x32_bf16 v[10:13], v[86:89], v[210:213], v[10:13]
	v_mfma_f32_16x16x32_bf16 v[54:57], v[146:149], v[162:165], 0
	v_mfma_f32_16x16x32_bf16 v[50:53], v[154:157], v[162:165], 0
	v_mfma_f32_16x16x32_bf16 v[38:41], v[146:149], v[184:187], 0
	v_mfma_f32_16x16x32_bf16 v[34:37], v[154:157], v[184:187], 0
	v_mfma_f32_16x16x32_bf16 v[22:25], v[146:149], v[192:195], 0
	v_mfma_f32_16x16x32_bf16 v[18:21], v[154:157], v[192:195], 0
	v_mfma_f32_16x16x32_bf16 v[6:9], v[146:149], v[206:209], 0
	v_mfma_f32_16x16x32_bf16 v[2:5], v[154:157], v[206:209], 0
	v_mfma_f32_16x16x32_bf16 v[54:57], v[150:153], v[166:169], v[54:57]
	v_mfma_f32_16x16x32_bf16 v[50:53], v[158:161], v[166:169], v[50:53]
	v_mfma_f32_16x16x32_bf16 v[38:41], v[150:153], v[188:191], v[38:41]
	v_mfma_f32_16x16x32_bf16 v[34:37], v[158:161], v[188:191], v[34:37]
	v_mfma_f32_16x16x32_bf16 v[22:25], v[150:153], v[202:205], v[22:25]
	v_mfma_f32_16x16x32_bf16 v[18:21], v[158:161], v[202:205], v[18:21]
	v_mfma_f32_16x16x32_bf16 v[6:9], v[150:153], v[210:213], v[6:9]
	v_mfma_f32_16x16x32_bf16 v[2:5], v[158:161], v[210:213], v[2:5]
	s_barrier
	s_add_i32 s74, 0, 0x18000
	s_add_i32 s75, 0, 0x1c000
	v_add_u32_e32 v86, s74, v197
	v_add_u32_e32 v158, s75, v197
	ds_read_b128 v[66:69], v86
	ds_read_b128 v[70:73], v86 offset:1024
	ds_read_b128 v[82:85], v86 offset:2048
	ds_read_b128 v[86:89], v86 offset:3072
	ds_read_b128 v[146:149], v158
	ds_read_b128 v[150:153], v158 offset:1024
	ds_read_b128 v[154:157], v158 offset:2048
	ds_read_b128 v[158:161], v158 offset:3072
	s_add_u32 s26, s58, 0x40000
	s_addc_u32 s27, s59, 0
	s_mov_b32 m0, s61
	v_lshl_add_u64 v[222:223], s[26:27], 0, v[172:173]
	ds_read_b128 v[162:165], v201 offset:32768
	ds_read_b128 v[166:169], v201 offset:33792
	ds_read_b128 v[184:187], v201 offset:34816
	ds_read_b128 v[188:191], v201 offset:35840
	ds_read_b128 v[192:195], v201 offset:36864
	ds_read_b128 v[202:205], v201 offset:37888
	ds_read_b128 v[206:209], v201 offset:38912
	ds_read_b128 v[210:213], v201 offset:39936
	global_load_lds_dwordx4 v[222:223], off
	v_lshl_add_u64 v[222:223], s[26:27], 0, v[174:175]
	s_mov_b32 m0, s62
	s_nop 0
	global_load_lds_dwordx4 v[222:223], off
	s_waitcnt vmcnt(8)
	s_waitcnt lgkmcnt(0)
	s_barrier
	v_mfma_f32_16x16x32_bf16 v[142:145], v[66:69], v[162:165], v[142:145]
	v_mfma_f32_16x16x32_bf16 v[138:141], v[82:85], v[162:165], v[138:141]
	v_mfma_f32_16x16x32_bf16 v[126:129], v[66:69], v[184:187], v[126:129]
	v_mfma_f32_16x16x32_bf16 v[122:125], v[82:85], v[184:187], v[122:125]
	v_mfma_f32_16x16x32_bf16 v[110:113], v[66:69], v[192:195], v[110:113]
	v_mfma_f32_16x16x32_bf16 v[106:109], v[82:85], v[192:195], v[106:109]
	v_mfma_f32_16x16x32_bf16 v[94:97], v[66:69], v[206:209], v[94:97]
	v_mfma_f32_16x16x32_bf16 v[90:93], v[82:85], v[206:209], v[90:93]
	v_mfma_f32_16x16x32_bf16 v[142:145], v[70:73], v[166:169], v[142:145]
	v_mfma_f32_16x16x32_bf16 v[138:141], v[86:89], v[166:169], v[138:141]
	v_mfma_f32_16x16x32_bf16 v[126:129], v[70:73], v[188:191], v[126:129]
	v_mfma_f32_16x16x32_bf16 v[122:125], v[86:89], v[188:191], v[122:125]
	v_mfma_f32_16x16x32_bf16 v[110:113], v[70:73], v[202:205], v[110:113]
	v_mfma_f32_16x16x32_bf16 v[106:109], v[86:89], v[202:205], v[106:109]
	v_mfma_f32_16x16x32_bf16 v[94:97], v[70:73], v[210:213], v[94:97]
	v_mfma_f32_16x16x32_bf16 v[90:93], v[86:89], v[210:213], v[90:93]
	v_mfma_f32_16x16x32_bf16 v[134:137], v[146:149], v[162:165], v[134:137]
	v_mfma_f32_16x16x32_bf16 v[130:133], v[154:157], v[162:165], v[130:133]
	v_mfma_f32_16x16x32_bf16 v[118:121], v[146:149], v[184:187], v[118:121]
	v_mfma_f32_16x16x32_bf16 v[114:117], v[154:157], v[184:187], v[114:117]
	v_mfma_f32_16x16x32_bf16 v[102:105], v[146:149], v[192:195], v[102:105]
	v_mfma_f32_16x16x32_bf16 v[98:101], v[154:157], v[192:195], v[98:101]
	v_mfma_f32_16x16x32_bf16 v[78:81], v[146:149], v[206:209], v[78:81]
	v_mfma_f32_16x16x32_bf16 v[74:77], v[154:157], v[206:209], v[74:77]
	v_mfma_f32_16x16x32_bf16 v[134:137], v[150:153], v[166:169], v[134:137]
	v_mfma_f32_16x16x32_bf16 v[130:133], v[158:161], v[166:169], v[130:133]
	v_mfma_f32_16x16x32_bf16 v[118:121], v[150:153], v[188:191], v[118:121]
	v_mfma_f32_16x16x32_bf16 v[114:117], v[158:161], v[188:191], v[114:117]
	v_mfma_f32_16x16x32_bf16 v[102:105], v[150:153], v[202:205], v[102:105]
	v_mfma_f32_16x16x32_bf16 v[98:101], v[158:161], v[202:205], v[98:101]
	v_mfma_f32_16x16x32_bf16 v[78:81], v[150:153], v[210:213], v[78:81]
	v_mfma_f32_16x16x32_bf16 v[74:77], v[158:161], v[210:213], v[74:77]
	s_barrier
	s_add_i32 s26, s74, s35
	v_lshl_add_u64 v[222:223], v[214:215], 0, s[16:17]
	s_mov_b32 m0, s26
	ds_read_b128 v[162:165], v201 offset:49152
	ds_read_b128 v[166:169], v201 offset:50176
	ds_read_b128 v[184:187], v201 offset:51200
	ds_read_b128 v[188:191], v201 offset:52224
	ds_read_b128 v[192:195], v201 offset:53248
	ds_read_b128 v[202:205], v201 offset:54272
	ds_read_b128 v[206:209], v201 offset:55296
	ds_read_b128 v[210:213], v201 offset:56320
	global_load_lds_dwordx4 v[222:223], off
	v_lshl_add_u64 v[222:223], v[214:215], 0, s[18:19]
	s_add_i32 m0, s26, 0x2000
	s_add_i32 s26, s75, s35
	global_load_lds_dwordx4 v[222:223], off
	v_lshl_add_u64 v[222:223], v[214:215], 0, s[22:23]
	s_mov_b32 m0, s26
	v_lshl_add_u64 v[214:215], v[214:215], 0, s[24:25]
	global_load_lds_dwordx4 v[222:223], off
	s_add_i32 m0, s26, 0x2000
	s_nop 0
	global_load_lds_dwordx4 v[214:215], off
	v_lshl_add_u64 v[214:215], v[216:217], 0, s[20:21]
	s_mov_b32 m0, s64
	s_nop 0
	global_load_lds_dwordx4 v[214:215], off
	v_lshl_add_u64 v[214:215], v[220:221], 0, s[20:21]
	s_mov_b32 m0, s65
	s_nop 0
	global_load_lds_dwordx4 v[214:215], off
	s_waitcnt vmcnt(8)
	s_waitcnt lgkmcnt(0)
	s_barrier
	v_mfma_f32_16x16x32_bf16 v[62:65], v[66:69], v[162:165], v[62:65]
	v_mfma_f32_16x16x32_bf16 v[58:61], v[82:85], v[162:165], v[58:61]
	v_mfma_f32_16x16x32_bf16 v[46:49], v[66:69], v[184:187], v[46:49]
	v_mfma_f32_16x16x32_bf16 v[42:45], v[82:85], v[184:187], v[42:45]
	v_mfma_f32_16x16x32_bf16 v[30:33], v[66:69], v[192:195], v[30:33]
	v_mfma_f32_16x16x32_bf16 v[26:29], v[82:85], v[192:195], v[26:29]
	v_mfma_f32_16x16x32_bf16 v[14:17], v[66:69], v[206:209], v[14:17]
	v_mfma_f32_16x16x32_bf16 v[10:13], v[82:85], v[206:209], v[10:13]
	v_mfma_f32_16x16x32_bf16 v[62:65], v[70:73], v[166:169], v[62:65]
	v_mfma_f32_16x16x32_bf16 v[58:61], v[86:89], v[166:169], v[58:61]
	v_mfma_f32_16x16x32_bf16 v[46:49], v[70:73], v[188:191], v[46:49]
	v_mfma_f32_16x16x32_bf16 v[42:45], v[86:89], v[188:191], v[42:45]
	v_mfma_f32_16x16x32_bf16 v[30:33], v[70:73], v[202:205], v[30:33]
	v_mfma_f32_16x16x32_bf16 v[26:29], v[86:89], v[202:205], v[26:29]
	v_mfma_f32_16x16x32_bf16 v[14:17], v[70:73], v[210:213], v[14:17]
	v_mfma_f32_16x16x32_bf16 v[10:13], v[86:89], v[210:213], v[10:13]
	v_mfma_f32_16x16x32_bf16 v[54:57], v[146:149], v[162:165], v[54:57]
	v_mfma_f32_16x16x32_bf16 v[50:53], v[154:157], v[162:165], v[50:53]
	v_mfma_f32_16x16x32_bf16 v[38:41], v[146:149], v[184:187], v[38:41]
	v_mfma_f32_16x16x32_bf16 v[34:37], v[154:157], v[184:187], v[34:37]
	v_mfma_f32_16x16x32_bf16 v[22:25], v[146:149], v[192:195], v[22:25]
	v_mfma_f32_16x16x32_bf16 v[18:21], v[154:157], v[192:195], v[18:21]
	v_mfma_f32_16x16x32_bf16 v[6:9], v[146:149], v[206:209], v[6:9]
	v_mfma_f32_16x16x32_bf16 v[2:5], v[154:157], v[206:209], v[2:5]
	v_mfma_f32_16x16x32_bf16 v[54:57], v[150:153], v[166:169], v[54:57]
	v_mfma_f32_16x16x32_bf16 v[50:53], v[158:161], v[166:169], v[50:53]
	v_mfma_f32_16x16x32_bf16 v[38:41], v[150:153], v[188:191], v[38:41]
	v_mfma_f32_16x16x32_bf16 v[34:37], v[158:161], v[188:191], v[34:37]
	v_mfma_f32_16x16x32_bf16 v[22:25], v[150:153], v[202:205], v[22:25]
	v_mfma_f32_16x16x32_bf16 v[18:21], v[158:161], v[202:205], v[18:21]
	v_mfma_f32_16x16x32_bf16 v[6:9], v[150:153], v[210:213], v[6:9]
	v_mfma_f32_16x16x32_bf16 v[2:5], v[158:161], v[210:213], v[2:5]
	s_barrier
	s_add_i32 s73, s73, 2
	s_add_u32 s71, s71, 0x10000
	s_addc_u32 s72, s72, 0
	s_add_u32 s56, s56, 0x100
	s_addc_u32 s57, s57, 0
	s_cmp_gt_u32 s73, 13

.LBB0_1270:
	s_ashr_i32 s51, s50, 31
	s_lshl_b64 s[26:27], s[50:51], 20
	v_readlane_b32 s52, v254, 58
	v_readlane_b32 s53, v254, 59
	s_add_u32 s52, s52, s26
	s_addc_u32 s53, s53, s27
	s_and_b64 s[26:27], s[0:1], exec
	s_cselect_b32 s51, s53, s61
	s_cselect_b32 s57, s52, s60
	s_ashr_i32 s45, s44, 31
	s_lshl_b64 s[26:27], s[44:45], 20
	s_add_u32 s54, s3, s26
	s_addc_u32 s55, s33, s27
	s_and_b64 s[26:27], s[0:1], exec
	s_cselect_b32 s45, s55, s59
	s_cselect_b32 s73, s54, s58
	s_add_u32 s74, s58, 0x10000
	s_addc_u32 s75, s59, 0
	s_add_u32 s58, s60, 0x80080
	s_addc_u32 s59, s61, 0
	s_mov_b32 s80, -2
	ds_read_b128 v[144:147], v158
	ds_read_b128 v[148:151], v158 offset:1024
	ds_read_b128 v[152:155], v158 offset:2048
	ds_read_b128 v[162:165], v158 offset:3072
	ds_read_b128 v[166:169], v159
	ds_read_b128 v[170:173], v159 offset:1024
	ds_read_b128 v[174:177], v159 offset:2048
	ds_read_b128 v[178:181], v159 offset:3072
	s_add_u32 s26, s58, 0xfff80080
	s_addc_u32 s27, s59, -1
	s_cmp_eq_u32 s80, 28
	s_cselect_b32 s61, s51, s27
	s_cselect_b32 s60, s57, s26
	s_cselect_b32 s27, s45, s75
	s_cselect_b32 s26, s73, s74
	v_lshl_add_u64 v[214:215], s[58:59], 0, v[136:137]
	s_add_i32 m0, s63, 0xc000
	ds_read_b128 v[182:185], v160
	ds_read_b128 v[186:189], v160 offset:1024
	ds_read_b128 v[190:193], v160 offset:2048
	ds_read_b128 v[194:197], v160 offset:3072
	ds_read_b128 v[198:201], v160 offset:4096
	ds_read_b128 v[202:205], v160 offset:5120
	ds_read_b128 v[206:209], v160 offset:6144
	ds_read_b128 v[210:213], v160 offset:7168
	global_load_lds_dwordx4 v[214:215], off
	v_lshl_add_u64 v[214:215], s[58:59], 0, v[138:139]
	s_add_i32 m0, s63, 0xe000
	s_nop 0
	global_load_lds_dwordx4 v[214:215], off
	s_waitcnt vmcnt(8)
	s_waitcnt lgkmcnt(0)
	s_barrier
	v_mfma_f32_16x16x32_bf16 v[126:129], v[144:147], v[182:185], 0
	v_mfma_f32_16x16x32_bf16 v[122:125], v[152:155], v[182:185], 0
	v_mfma_f32_16x16x32_bf16 v[118:121], v[144:147], v[190:193], 0
	v_mfma_f32_16x16x32_bf16 v[114:117], v[152:155], v[190:193], 0
	v_mfma_f32_16x16x32_bf16 v[106:109], v[144:147], v[198:201], 0
	v_mfma_f32_16x16x32_bf16 v[98:101], v[152:155], v[198:201], 0
	v_mfma_f32_16x16x32_bf16 v[90:93], v[144:147], v[206:209], 0
	v_mfma_f32_16x16x32_bf16 v[82:85], v[152:155], v[206:209], 0
	v_mfma_f32_16x16x32_bf16 v[126:129], v[148:151], v[186:189], v[126:129]
	v_mfma_f32_16x16x32_bf16 v[122:125], v[162:165], v[186:189], v[122:125]
	v_mfma_f32_16x16x32_bf16 v[118:121], v[148:151], v[194:197], v[118:121]
	v_mfma_f32_16x16x32_bf16 v[114:117], v[162:165], v[194:197], v[114:117]
	v_mfma_f32_16x16x32_bf16 v[106:109], v[148:151], v[202:205], v[106:109]
	v_mfma_f32_16x16x32_bf16 v[98:101], v[162:165], v[202:205], v[98:101]
	v_mfma_f32_16x16x32_bf16 v[90:93], v[148:151], v[210:213], v[90:93]
	v_mfma_f32_16x16x32_bf16 v[82:85], v[162:165], v[210:213], v[82:85]
	v_mfma_f32_16x16x32_bf16 v[110:113], v[166:169], v[182:185], 0
	v_mfma_f32_16x16x32_bf16 v[102:105], v[174:177], v[182:185], 0
	v_mfma_f32_16x16x32_bf16 v[94:97], v[166:169], v[190:193], 0
	v_mfma_f32_16x16x32_bf16 v[86:89], v[174:177], v[190:193], 0
	v_mfma_f32_16x16x32_bf16 v[78:81], v[166:169], v[198:201], 0
	v_mfma_f32_16x16x32_bf16 v[74:77], v[174:177], v[198:201], 0
	v_mfma_f32_16x16x32_bf16 v[70:73], v[166:169], v[206:209], 0
	v_mfma_f32_16x16x32_bf16 v[66:69], v[174:177], v[206:209], 0
	v_mfma_f32_16x16x32_bf16 v[110:113], v[170:173], v[186:189], v[110:113]
	v_mfma_f32_16x16x32_bf16 v[102:105], v[178:181], v[186:189], v[102:105]
	v_mfma_f32_16x16x32_bf16 v[94:97], v[170:173], v[194:197], v[94:97]
	v_mfma_f32_16x16x32_bf16 v[86:89], v[178:181], v[194:197], v[86:89]
	v_mfma_f32_16x16x32_bf16 v[78:81], v[170:173], v[202:205], v[78:81]
	v_mfma_f32_16x16x32_bf16 v[74:77], v[178:181], v[202:205], v[74:77]
	v_mfma_f32_16x16x32_bf16 v[70:73], v[170:173], v[210:213], v[70:73]
	v_mfma_f32_16x16x32_bf16 v[66:69], v[178:181], v[210:213], v[66:69]
	s_barrier
	v_lshl_add_u64 v[214:215], s[26:27], 0, v[130:131]
	s_add_i32 s26, s71, s35
	s_mov_b32 m0, s26
	ds_read_b128 v[182:185], v160 offset:16384
	ds_read_b128 v[186:189], v160 offset:17408
	ds_read_b128 v[190:193], v160 offset:18432
	ds_read_b128 v[194:197], v160 offset:19456
	ds_read_b128 v[198:201], v160 offset:20480
	ds_read_b128 v[202:205], v160 offset:21504
	ds_read_b128 v[206:209], v160 offset:22528
	ds_read_b128 v[210:213], v160 offset:23552
	global_load_lds_dwordx4 v[214:215], off
	v_lshl_add_u64 v[216:217], v[214:215], 0, s[6:7]
	s_add_i32 m0, s26, 0x2000
	s_add_i32 s26, s72, s35
	global_load_lds_dwordx4 v[216:217], off
	v_lshl_add_u64 v[216:217], v[214:215], 0, s[8:9]
	s_mov_b32 m0, s26
	v_lshl_add_u64 v[220:221], s[60:61], 0, v[134:135]
	global_load_lds_dwordx4 v[216:217], off
	v_lshl_add_u64 v[216:217], v[214:215], 0, s[10:11]
	s_add_i32 m0, s26, 0x2000
	s_nop 0
	global_load_lds_dwordx4 v[216:217], off
	v_lshl_add_u64 v[216:217], s[60:61], 0, v[132:133]
	s_mov_b32 m0, s63
	s_nop 0
	global_load_lds_dwordx4 v[216:217], off
	s_mov_b32 m0, s64
	s_nop 0
	global_load_lds_dwordx4 v[220:221], off
	s_waitcnt vmcnt(8)
	s_waitcnt lgkmcnt(0)
	s_barrier
	v_mfma_f32_16x16x32_bf16 v[62:65], v[144:147], v[182:185], 0
	v_mfma_f32_16x16x32_bf16 v[58:61], v[152:155], v[182:185], 0
	v_mfma_f32_16x16x32_bf16 v[54:57], v[144:147], v[190:193], 0
	v_mfma_f32_16x16x32_bf16 v[46:49], v[152:155], v[190:193], 0
	v_mfma_f32_16x16x32_bf16 v[38:41], v[144:147], v[198:201], 0
	v_mfma_f32_16x16x32_bf16 v[30:33], v[152:155], v[198:201], 0
	v_mfma_f32_16x16x32_bf16 v[22:25], v[144:147], v[206:209], 0
	v_mfma_f32_16x16x32_bf16 v[14:17], v[152:155], v[206:209], 0
	v_mfma_f32_16x16x32_bf16 v[62:65], v[148:151], v[186:189], v[62:65]
	v_mfma_f32_16x16x32_bf16 v[58:61], v[162:165], v[186:189], v[58:61]
	v_mfma_f32_16x16x32_bf16 v[54:57], v[148:151], v[194:197], v[54:57]
	v_mfma_f32_16x16x32_bf16 v[46:49], v[162:165], v[194:197], v[46:49]
	v_mfma_f32_16x16x32_bf16 v[38:41], v[148:151], v[202:205], v[38:41]
	v_mfma_f32_16x16x32_bf16 v[30:33], v[162:165], v[202:205], v[30:33]
	v_mfma_f32_16x16x32_bf16 v[22:25], v[148:151], v[210:213], v[22:25]
	v_mfma_f32_16x16x32_bf16 v[14:17], v[162:165], v[210:213], v[14:17]
	v_mfma_f32_16x16x32_bf16 v[50:53], v[166:169], v[182:185], 0
	v_mfma_f32_16x16x32_bf16 v[42:45], v[174:177], v[182:185], 0
	v_mfma_f32_16x16x32_bf16 v[34:37], v[166:169], v[190:193], 0
	v_mfma_f32_16x16x32_bf16 v[26:29], v[174:177], v[190:193], 0
	v_mfma_f32_16x16x32_bf16 v[18:21], v[166:169], v[198:201], 0
	v_mfma_f32_16x16x32_bf16 v[10:13], v[174:177], v[198:201], 0
	v_mfma_f32_16x16x32_bf16 v[6:9], v[166:169], v[206:209], 0
	v_mfma_f32_16x16x32_bf16 v[2:5], v[174:177], v[206:209], 0
	v_mfma_f32_16x16x32_bf16 v[50:53], v[170:173], v[186:189], v[50:53]
	v_mfma_f32_16x16x32_bf16 v[42:45], v[178:181], v[186:189], v[42:45]
	v_mfma_f32_16x16x32_bf16 v[34:37], v[170:173], v[194:197], v[34:37]
	v_mfma_f32_16x16x32_bf16 v[26:29], v[178:181], v[194:197], v[26:29]
	v_mfma_f32_16x16x32_bf16 v[18:21], v[170:173], v[202:205], v[18:21]
	v_mfma_f32_16x16x32_bf16 v[10:13], v[178:181], v[202:205], v[10:13]
	v_mfma_f32_16x16x32_bf16 v[6:9], v[170:173], v[210:213], v[6:9]
	v_mfma_f32_16x16x32_bf16 v[2:5], v[178:181], v[210:213], v[2:5]
	s_barrier
	s_add_i32 s81, 0, 0x18000
	v_add_u32_e32 v161, s81, v156
	s_add_i32 s82, 0, 0x1c000
	ds_read_b128 v[144:147], v161
	ds_read_b128 v[148:151], v161 offset:1024
	ds_read_b128 v[152:155], v161 offset:2048
	ds_read_b128 v[162:165], v161 offset:3072
	v_add_u32_e32 v161, s82, v156
	ds_read_b128 v[166:169], v161
	ds_read_b128 v[170:173], v161 offset:1024
	ds_read_b128 v[174:177], v161 offset:2048
	ds_read_b128 v[178:181], v161 offset:3072
	s_add_u32 s26, s60, 0x80000
	s_addc_u32 s27, s61, 0
	s_mov_b32 m0, s65
	v_lshl_add_u64 v[222:223], s[26:27], 0, v[132:133]
	ds_read_b128 v[182:185], v160 offset:32768
	ds_read_b128 v[186:189], v160 offset:33792
	ds_read_b128 v[190:193], v160 offset:34816
	ds_read_b128 v[194:197], v160 offset:35840
	ds_read_b128 v[198:201], v160 offset:36864
	ds_read_b128 v[202:205], v160 offset:37888
	ds_read_b128 v[206:209], v160 offset:38912
	ds_read_b128 v[210:213], v160 offset:39936
	global_load_lds_dwordx4 v[222:223], off
	v_lshl_add_u64 v[222:223], s[26:27], 0, v[134:135]
	s_mov_b32 m0, s66
	s_nop 0
	global_load_lds_dwordx4 v[222:223], off
	s_waitcnt vmcnt(8)
	s_waitcnt lgkmcnt(0)
	s_barrier
	v_mfma_f32_16x16x32_bf16 v[126:129], v[144:147], v[182:185], v[126:129]
	v_mfma_f32_16x16x32_bf16 v[122:125], v[152:155], v[182:185], v[122:125]
	v_mfma_f32_16x16x32_bf16 v[118:121], v[144:147], v[190:193], v[118:121]
	v_mfma_f32_16x16x32_bf16 v[114:117], v[152:155], v[190:193], v[114:117]
	v_mfma_f32_16x16x32_bf16 v[106:109], v[144:147], v[198:201], v[106:109]
	v_mfma_f32_16x16x32_bf16 v[98:101], v[152:155], v[198:201], v[98:101]
	v_mfma_f32_16x16x32_bf16 v[90:93], v[144:147], v[206:209], v[90:93]
	v_mfma_f32_16x16x32_bf16 v[82:85], v[152:155], v[206:209], v[82:85]
	v_mfma_f32_16x16x32_bf16 v[126:129], v[148:151], v[186:189], v[126:129]
	v_mfma_f32_16x16x32_bf16 v[122:125], v[162:165], v[186:189], v[122:125]
	v_mfma_f32_16x16x32_bf16 v[118:121], v[148:151], v[194:197], v[118:121]
	v_mfma_f32_16x16x32_bf16 v[114:117], v[162:165], v[194:197], v[114:117]
	v_mfma_f32_16x16x32_bf16 v[106:109], v[148:151], v[202:205], v[106:109]
	v_mfma_f32_16x16x32_bf16 v[98:101], v[162:165], v[202:205], v[98:101]
	v_mfma_f32_16x16x32_bf16 v[90:93], v[148:151], v[210:213], v[90:93]
	v_mfma_f32_16x16x32_bf16 v[82:85], v[162:165], v[210:213], v[82:85]
	v_mfma_f32_16x16x32_bf16 v[110:113], v[166:169], v[182:185], v[110:113]
	v_mfma_f32_16x16x32_bf16 v[102:105], v[174:177], v[182:185], v[102:105]
	v_mfma_f32_16x16x32_bf16 v[94:97], v[166:169], v[190:193], v[94:97]
	v_mfma_f32_16x16x32_bf16 v[86:89], v[174:177], v[190:193], v[86:89]
	v_mfma_f32_16x16x32_bf16 v[78:81], v[166:169], v[198:201], v[78:81]
	v_mfma_f32_16x16x32_bf16 v[74:77], v[174:177], v[198:201], v[74:77]
	v_mfma_f32_16x16x32_bf16 v[70:73], v[166:169], v[206:209], v[70:73]
	v_mfma_f32_16x16x32_bf16 v[66:69], v[174:177], v[206:209], v[66:69]
	v_mfma_f32_16x16x32_bf16 v[110:113], v[170:173], v[186:189], v[110:113]
	v_mfma_f32_16x16x32_bf16 v[102:105], v[178:181], v[186:189], v[102:105]
	v_mfma_f32_16x16x32_bf16 v[94:97], v[170:173], v[194:197], v[94:97]
	v_mfma_f32_16x16x32_bf16 v[86:89], v[178:181], v[194:197], v[86:89]
	v_mfma_f32_16x16x32_bf16 v[78:81], v[170:173], v[202:205], v[78:81]
	v_mfma_f32_16x16x32_bf16 v[74:77], v[178:181], v[202:205], v[74:77]
	v_mfma_f32_16x16x32_bf16 v[70:73], v[170:173], v[210:213], v[70:73]
	v_mfma_f32_16x16x32_bf16 v[66:69], v[178:181], v[210:213], v[66:69]
	s_barrier
	s_add_i32 s26, s81, s35
	v_lshl_add_u64 v[222:223], v[214:215], 0, s[14:15]
	s_mov_b32 m0, s26
	ds_read_b128 v[182:185], v160 offset:49152
	ds_read_b128 v[186:189], v160 offset:50176
	ds_read_b128 v[190:193], v160 offset:51200
	ds_read_b128 v[194:197], v160 offset:52224
	ds_read_b128 v[198:201], v160 offset:53248
	ds_read_b128 v[202:205], v160 offset:54272
	ds_read_b128 v[206:209], v160 offset:55296
	ds_read_b128 v[210:213], v160 offset:56320
	global_load_lds_dwordx4 v[222:223], off
	v_lshl_add_u64 v[222:223], v[214:215], 0, s[16:17]
	s_add_i32 m0, s26, 0x2000
	s_add_i32 s26, s82, s35
	global_load_lds_dwordx4 v[222:223], off
	v_lshl_add_u64 v[222:223], v[214:215], 0, s[20:21]
	s_mov_b32 m0, s26
	v_lshl_add_u64 v[214:215], v[214:215], 0, s[22:23]
	global_load_lds_dwordx4 v[222:223], off
	s_add_i32 m0, s26, 0x2000
	s_nop 0
	global_load_lds_dwordx4 v[214:215], off
	v_lshl_add_u64 v[214:215], v[216:217], 0, s[18:19]
	s_mov_b32 m0, s68
	s_nop 0
	global_load_lds_dwordx4 v[214:215], off
	v_lshl_add_u64 v[214:215], v[220:221], 0, s[18:19]
	s_mov_b32 m0, s69
	s_nop 0
	global_load_lds_dwordx4 v[214:215], off
	s_waitcnt vmcnt(8)
	s_waitcnt lgkmcnt(0)
	s_barrier
	v_mfma_f32_16x16x32_bf16 v[62:65], v[144:147], v[182:185], v[62:65]
	v_mfma_f32_16x16x32_bf16 v[58:61], v[152:155], v[182:185], v[58:61]
	v_mfma_f32_16x16x32_bf16 v[54:57], v[144:147], v[190:193], v[54:57]
	v_mfma_f32_16x16x32_bf16 v[46:49], v[152:155], v[190:193], v[46:49]
	v_mfma_f32_16x16x32_bf16 v[38:41], v[144:147], v[198:201], v[38:41]
	v_mfma_f32_16x16x32_bf16 v[30:33], v[152:155], v[198:201], v[30:33]
	v_mfma_f32_16x16x32_bf16 v[22:25], v[144:147], v[206:209], v[22:25]
	v_mfma_f32_16x16x32_bf16 v[14:17], v[152:155], v[206:209], v[14:17]
	v_mfma_f32_16x16x32_bf16 v[62:65], v[148:151], v[186:189], v[62:65]
	v_mfma_f32_16x16x32_bf16 v[58:61], v[162:165], v[186:189], v[58:61]
	v_mfma_f32_16x16x32_bf16 v[54:57], v[148:151], v[194:197], v[54:57]
	v_mfma_f32_16x16x32_bf16 v[46:49], v[162:165], v[194:197], v[46:49]
	v_mfma_f32_16x16x32_bf16 v[38:41], v[148:151], v[202:205], v[38:41]
	v_mfma_f32_16x16x32_bf16 v[30:33], v[162:165], v[202:205], v[30:33]
	v_mfma_f32_16x16x32_bf16 v[22:25], v[148:151], v[210:213], v[22:25]
	v_mfma_f32_16x16x32_bf16 v[14:17], v[162:165], v[210:213], v[14:17]
	v_mfma_f32_16x16x32_bf16 v[50:53], v[166:169], v[182:185], v[50:53]
	v_mfma_f32_16x16x32_bf16 v[42:45], v[174:177], v[182:185], v[42:45]
	v_mfma_f32_16x16x32_bf16 v[34:37], v[166:169], v[190:193], v[34:37]
	v_mfma_f32_16x16x32_bf16 v[26:29], v[174:177], v[190:193], v[26:29]
	v_mfma_f32_16x16x32_bf16 v[18:21], v[166:169], v[198:201], v[18:21]
	v_mfma_f32_16x16x32_bf16 v[10:13], v[174:177], v[198:201], v[10:13]
	v_mfma_f32_16x16x32_bf16 v[6:9], v[166:169], v[206:209], v[6:9]
	v_mfma_f32_16x16x32_bf16 v[2:5], v[174:177], v[206:209], v[2:5]
	v_mfma_f32_16x16x32_bf16 v[50:53], v[170:173], v[186:189], v[50:53]
	v_mfma_f32_16x16x32_bf16 v[42:45], v[178:181], v[186:189], v[42:45]
	v_mfma_f32_16x16x32_bf16 v[34:37], v[170:173], v[194:197], v[34:37]
	v_mfma_f32_16x16x32_bf16 v[26:29], v[178:181], v[194:197], v[26:29]
	v_mfma_f32_16x16x32_bf16 v[18:21], v[170:173], v[202:205], v[18:21]
	v_mfma_f32_16x16x32_bf16 v[10:13], v[178:181], v[202:205], v[10:13]
	v_mfma_f32_16x16x32_bf16 v[6:9], v[170:173], v[210:213], v[6:9]
	v_mfma_f32_16x16x32_bf16 v[2:5], v[178:181], v[210:213], v[2:5]
	s_barrier
	s_add_i32 s80, s80, 2
	s_add_u32 s74, s74, 0x10000
	s_addc_u32 s75, s75, 0
	s_add_u32 s58, s58, 0x100
	s_addc_u32 s59, s59, 0
	s_cmp_gt_u32 s80, 29

.LBB0_1496:
	s_lshl_b64 s[50:51], s[48:49], 19
	s_add_u32 s50, s59, s50
	s_addc_u32 s51, s60, s51
	s_and_b64 s[4:5], s[4:5], exec
	s_cselect_b32 s2, s51, s57
	s_cselect_b32 s47, s50, s56
	s_add_u32 s4, s56, 0x40080
	v_lshl_add_u64 v[176:177], v[2:3], 0, s[40:41]
	s_addc_u32 s5, s57, 0
	s_mov_b32 s49, -2
	ds_read_b128 v[26:29], v186
	ds_read_b128 v[30:33], v186 offset:1024
	ds_read_b128 v[18:21], v186 offset:2048
	ds_read_b128 v[22:25], v186 offset:3072
	ds_read_b128 v[10:13], v187
	ds_read_b128 v[14:17], v187 offset:1024
	ds_read_b128 v[2:5], v187 offset:2048
	ds_read_b128 v[6:9], v187 offset:3072
	s_add_u32 s56, s4, 0xfffc0080
	s_addc_u32 s57, s5, -1
	s_cmp_eq_u32 s49, 12
	s_cselect_b64 vcc, -1, 0
	s_cselect_b32 s57, s2, s57
	s_cselect_b32 s56, s47, s56
	v_cndmask_b32_e32 v179, v177, v175, vcc
	v_cndmask_b32_e32 v178, v176, v174, vcc
	v_lshl_add_u64 v[180:181], s[4:5], 0, v[168:169]
	s_add_i32 m0, s62, 0xc000
	ds_read_b128 v[192:195], v188
	ds_read_b128 v[196:199], v188 offset:1024
	ds_read_b128 v[200:203], v188 offset:2048
	ds_read_b128 v[204:207], v188 offset:3072
	ds_read_b128 v[208:211], v188 offset:4096
	ds_read_b128 v[212:215], v188 offset:5120
	ds_read_b128 v[220:223], v188 offset:6144
	ds_read_b128 v[224:227], v188 offset:7168
	global_load_lds_dwordx4 v[180:181], off
	v_lshl_add_u64 v[180:181], s[4:5], 0, v[170:171]
	s_add_i32 m0, s62, 0xe000
	s_nop 0
	global_load_lds_dwordx4 v[180:181], off
	s_waitcnt vmcnt(16)
	s_waitcnt lgkmcnt(0)
	s_barrier
	v_mfma_scale_f32_16x16x128_f8f6f4 v[158:161], v[26:33], v[192:199], 0, v189, v190 op_sel_hi:[0,0,0]
	v_mfma_scale_f32_16x16x128_f8f6f4 v[150:153], v[18:25], v[192:199], 0, v189, v190 op_sel_hi:[0,0,0]
	v_mfma_scale_f32_16x16x128_f8f6f4 v[142:145], v[26:33], v[200:207], 0, v189, v190 op_sel_hi:[0,0,0]
	v_mfma_scale_f32_16x16x128_f8f6f4 v[134:137], v[18:25], v[200:207], 0, v189, v190 op_sel_hi:[0,0,0]
	v_mfma_scale_f32_16x16x128_f8f6f4 v[126:129], v[26:33], v[208:215], 0, v189, v190 op_sel_hi:[0,0,0]
	v_mfma_scale_f32_16x16x128_f8f6f4 v[118:121], v[18:25], v[208:215], 0, v189, v190 op_sel_hi:[0,0,0]
	v_mfma_scale_f32_16x16x128_f8f6f4 v[110:113], v[26:33], v[220:227], 0, v189, v190 op_sel_hi:[0,0,0]
	v_mfma_scale_f32_16x16x128_f8f6f4 v[102:105], v[18:25], v[220:227], 0, v189, v190 op_sel_hi:[0,0,0]
	v_mfma_scale_f32_16x16x128_f8f6f4 v[154:157], v[10:17], v[192:199], 0, v189, v190 op_sel_hi:[0,0,0]
	v_mfma_scale_f32_16x16x128_f8f6f4 v[146:149], v[2:9], v[192:199], 0, v189, v190 op_sel_hi:[0,0,0]
	v_mfma_scale_f32_16x16x128_f8f6f4 v[138:141], v[10:17], v[200:207], 0, v189, v190 op_sel_hi:[0,0,0]
	v_mfma_scale_f32_16x16x128_f8f6f4 v[130:133], v[2:9], v[200:207], 0, v189, v190 op_sel_hi:[0,0,0]
	v_mfma_scale_f32_16x16x128_f8f6f4 v[122:125], v[10:17], v[208:215], 0, v189, v190 op_sel_hi:[0,0,0]
	v_mfma_scale_f32_16x16x128_f8f6f4 v[114:117], v[2:9], v[208:215], 0, v189, v190 op_sel_hi:[0,0,0]
	v_mfma_scale_f32_16x16x128_f8f6f4 v[106:109], v[10:17], v[220:227], 0, v189, v190 op_sel_hi:[0,0,0]
	v_mfma_scale_f32_16x16x128_f8f6f4 v[98:101], v[2:9], v[220:227], 0, v189, v190 op_sel_hi:[0,0,0]
	s_barrier
	s_add_i32 s73, s69, s61
	v_lshl_add_u64 v[178:179], v[178:179], 0, v[162:163]
	s_mov_b32 m0, s73
	ds_read_b128 v[192:195], v188 offset:16384
	ds_read_b128 v[196:199], v188 offset:17408
	ds_read_b128 v[200:203], v188 offset:18432
	ds_read_b128 v[204:207], v188 offset:19456
	ds_read_b128 v[208:211], v188 offset:20480
	ds_read_b128 v[212:215], v188 offset:21504
	ds_read_b128 v[220:223], v188 offset:22528
	ds_read_b128 v[224:227], v188 offset:23552
	global_load_lds_dwordx4 v[178:179], off
	v_lshl_add_u64 v[180:181], v[178:179], 0, s[10:11]
	s_add_i32 m0, s73, 0x2000
	s_add_i32 s73, s70, s61
	global_load_lds_dwordx4 v[180:181], off
	v_lshl_add_u64 v[180:181], v[178:179], 0, s[12:13]
	s_mov_b32 m0, s73
	v_lshl_add_u64 v[182:183], s[56:57], 0, v[166:167]
	global_load_lds_dwordx4 v[180:181], off
	v_lshl_add_u64 v[180:181], v[178:179], 0, s[14:15]
	s_add_i32 m0, s73, 0x2000
	s_nop 0
	global_load_lds_dwordx4 v[180:181], off
	v_lshl_add_u64 v[180:181], s[56:57], 0, v[164:165]
	s_mov_b32 m0, s62
	s_nop 0
	global_load_lds_dwordx4 v[180:181], off
	s_mov_b32 m0, s53
	s_nop 0
	global_load_lds_dwordx4 v[182:183], off
	s_waitcnt vmcnt(16)
	s_waitcnt lgkmcnt(0)
	s_barrier
	v_mfma_scale_f32_16x16x128_f8f6f4 v[94:97], v[26:33], v[192:199], 0, v189, v190 op_sel_hi:[0,0,0]
	v_mfma_scale_f32_16x16x128_f8f6f4 v[86:89], v[18:25], v[192:199], 0, v189, v190 op_sel_hi:[0,0,0]
	v_mfma_scale_f32_16x16x128_f8f6f4 v[78:81], v[26:33], v[200:207], 0, v189, v190 op_sel_hi:[0,0,0]
	v_mfma_scale_f32_16x16x128_f8f6f4 v[70:73], v[18:25], v[200:207], 0, v189, v190 op_sel_hi:[0,0,0]
	v_mfma_scale_f32_16x16x128_f8f6f4 v[62:65], v[26:33], v[208:215], 0, v189, v190 op_sel_hi:[0,0,0]
	v_mfma_scale_f32_16x16x128_f8f6f4 v[54:57], v[18:25], v[208:215], 0, v189, v190 op_sel_hi:[0,0,0]
	v_mfma_scale_f32_16x16x128_f8f6f4 v[46:49], v[26:33], v[220:227], 0, v189, v190 op_sel_hi:[0,0,0]
	v_mfma_scale_f32_16x16x128_f8f6f4 v[38:41], v[18:25], v[220:227], 0, v189, v190 op_sel_hi:[0,0,0]
	v_mfma_scale_f32_16x16x128_f8f6f4 v[90:93], v[10:17], v[192:199], 0, v189, v190 op_sel_hi:[0,0,0]
	v_mfma_scale_f32_16x16x128_f8f6f4 v[82:85], v[2:9], v[192:199], 0, v189, v190 op_sel_hi:[0,0,0]
	v_mfma_scale_f32_16x16x128_f8f6f4 v[74:77], v[10:17], v[200:207], 0, v189, v190 op_sel_hi:[0,0,0]
	v_mfma_scale_f32_16x16x128_f8f6f4 v[66:69], v[2:9], v[200:207], 0, v189, v190 op_sel_hi:[0,0,0]
	v_mfma_scale_f32_16x16x128_f8f6f4 v[58:61], v[10:17], v[208:215], 0, v189, v190 op_sel_hi:[0,0,0]
	v_mfma_scale_f32_16x16x128_f8f6f4 v[50:53], v[2:9], v[208:215], 0, v189, v190 op_sel_hi:[0,0,0]
	v_mfma_scale_f32_16x16x128_f8f6f4 v[42:45], v[10:17], v[220:227], 0, v189, v190 op_sel_hi:[0,0,0]
	v_mfma_scale_f32_16x16x128_f8f6f4 v[34:37], v[2:9], v[220:227], 0, v189, v190 op_sel_hi:[0,0,0]
	s_barrier
	s_add_i32 s73, 0, 0x18000
	s_add_i32 s74, 0, 0x1c000
	v_add_u32_e32 v14, s73, v184
	v_add_u32_e32 v30, s74, v184
	ds_read_b128 v[2:5], v14
	ds_read_b128 v[6:9], v14 offset:1024
	ds_read_b128 v[10:13], v14 offset:2048
	ds_read_b128 v[14:17], v14 offset:3072
	ds_read_b128 v[18:21], v30
	ds_read_b128 v[22:25], v30 offset:1024
	ds_read_b128 v[26:29], v30 offset:2048
	ds_read_b128 v[30:33], v30 offset:3072
	s_add_u32 s56, s56, 0x40000
	s_addc_u32 s57, s57, 0
	s_mov_b32 m0, s63
	v_lshl_add_u64 v[216:217], s[56:57], 0, v[164:165]
	ds_read_b128 v[192:195], v188 offset:32768
	ds_read_b128 v[196:199], v188 offset:33792
	ds_read_b128 v[200:203], v188 offset:34816
	ds_read_b128 v[204:207], v188 offset:35840
	ds_read_b128 v[208:211], v188 offset:36864
	ds_read_b128 v[212:215], v188 offset:37888
	ds_read_b128 v[220:223], v188 offset:38912
	ds_read_b128 v[224:227], v188 offset:39936
	global_load_lds_dwordx4 v[216:217], off
	v_lshl_add_u64 v[216:217], s[56:57], 0, v[166:167]
	s_mov_b32 m0, s64
	s_nop 0
	global_load_lds_dwordx4 v[216:217], off
	s_waitcnt vmcnt(8)
	s_waitcnt lgkmcnt(0)
	s_barrier
	v_mfma_scale_f32_16x16x128_f8f6f4 v[158:161], v[2:9], v[192:199], v[158:161], v189, v190 op_sel_hi:[0,0,0]
	v_mfma_scale_f32_16x16x128_f8f6f4 v[150:153], v[10:17], v[192:199], v[150:153], v189, v190 op_sel_hi:[0,0,0]
	v_mfma_scale_f32_16x16x128_f8f6f4 v[142:145], v[2:9], v[200:207], v[142:145], v189, v190 op_sel_hi:[0,0,0]
	v_mfma_scale_f32_16x16x128_f8f6f4 v[134:137], v[10:17], v[200:207], v[134:137], v189, v190 op_sel_hi:[0,0,0]
	v_mfma_scale_f32_16x16x128_f8f6f4 v[126:129], v[2:9], v[208:215], v[126:129], v189, v190 op_sel_hi:[0,0,0]
	v_mfma_scale_f32_16x16x128_f8f6f4 v[118:121], v[10:17], v[208:215], v[118:121], v189, v190 op_sel_hi:[0,0,0]
	v_mfma_scale_f32_16x16x128_f8f6f4 v[110:113], v[2:9], v[220:227], v[110:113], v189, v190 op_sel_hi:[0,0,0]
	v_mfma_scale_f32_16x16x128_f8f6f4 v[102:105], v[10:17], v[220:227], v[102:105], v189, v190 op_sel_hi:[0,0,0]
	v_mfma_scale_f32_16x16x128_f8f6f4 v[154:157], v[18:25], v[192:199], v[154:157], v189, v190 op_sel_hi:[0,0,0]
	v_mfma_scale_f32_16x16x128_f8f6f4 v[146:149], v[26:33], v[192:199], v[146:149], v189, v190 op_sel_hi:[0,0,0]
	v_mfma_scale_f32_16x16x128_f8f6f4 v[138:141], v[18:25], v[200:207], v[138:141], v189, v190 op_sel_hi:[0,0,0]
	v_mfma_scale_f32_16x16x128_f8f6f4 v[130:133], v[26:33], v[200:207], v[130:133], v189, v190 op_sel_hi:[0,0,0]
	v_mfma_scale_f32_16x16x128_f8f6f4 v[122:125], v[18:25], v[208:215], v[122:125], v189, v190 op_sel_hi:[0,0,0]
	v_mfma_scale_f32_16x16x128_f8f6f4 v[114:117], v[26:33], v[208:215], v[114:117], v189, v190 op_sel_hi:[0,0,0]
	v_mfma_scale_f32_16x16x128_f8f6f4 v[106:109], v[18:25], v[220:227], v[106:109], v189, v190 op_sel_hi:[0,0,0]
	v_mfma_scale_f32_16x16x128_f8f6f4 v[98:101], v[26:33], v[220:227], v[98:101], v189, v190 op_sel_hi:[0,0,0]
	s_barrier
	s_add_i32 s56, s73, s61
	v_lshl_add_u64 v[216:217], v[178:179], 0, s[20:21]
	s_mov_b32 m0, s56
	ds_read_b128 v[192:195], v188 offset:49152
	ds_read_b128 v[196:199], v188 offset:50176
	ds_read_b128 v[200:203], v188 offset:51200
	ds_read_b128 v[204:207], v188 offset:52224
	ds_read_b128 v[208:211], v188 offset:53248
	ds_read_b128 v[212:215], v188 offset:54272
	ds_read_b128 v[220:223], v188 offset:55296
	ds_read_b128 v[224:227], v188 offset:56320
	global_load_lds_dwordx4 v[216:217], off
	v_lshl_add_u64 v[216:217], v[178:179], 0, s[22:23]
	s_add_i32 m0, s56, 0x2000
	s_add_i32 s56, s74, s61
	global_load_lds_dwordx4 v[216:217], off
	v_lshl_add_u64 v[216:217], v[178:179], 0, s[26:27]
	s_mov_b32 m0, s56
	v_lshl_add_u64 v[178:179], v[178:179], 0, s[36:37]
	global_load_lds_dwordx4 v[216:217], off
	s_add_i32 m0, s56, 0x2000
	s_nop 0
	global_load_lds_dwordx4 v[178:179], off
	v_lshl_add_u64 v[178:179], v[180:181], 0, s[24:25]
	s_mov_b32 m0, s66
	s_nop 0
	global_load_lds_dwordx4 v[178:179], off
	v_lshl_add_u64 v[178:179], v[182:183], 0, s[24:25]
	s_mov_b32 m0, s67
	s_nop 0
	global_load_lds_dwordx4 v[178:179], off
	s_waitcnt vmcnt(8)
	s_waitcnt lgkmcnt(0)
	s_barrier
	v_mfma_scale_f32_16x16x128_f8f6f4 v[94:97], v[2:9], v[192:199], v[94:97], v189, v190 op_sel_hi:[0,0,0]
	v_mfma_scale_f32_16x16x128_f8f6f4 v[86:89], v[10:17], v[192:199], v[86:89], v189, v190 op_sel_hi:[0,0,0]
	v_mfma_scale_f32_16x16x128_f8f6f4 v[78:81], v[2:9], v[200:207], v[78:81], v189, v190 op_sel_hi:[0,0,0]
	v_mfma_scale_f32_16x16x128_f8f6f4 v[70:73], v[10:17], v[200:207], v[70:73], v189, v190 op_sel_hi:[0,0,0]
	v_mfma_scale_f32_16x16x128_f8f6f4 v[62:65], v[2:9], v[208:215], v[62:65], v189, v190 op_sel_hi:[0,0,0]
	v_mfma_scale_f32_16x16x128_f8f6f4 v[54:57], v[10:17], v[208:215], v[54:57], v189, v190 op_sel_hi:[0,0,0]
	v_mfma_scale_f32_16x16x128_f8f6f4 v[46:49], v[2:9], v[220:227], v[46:49], v189, v190 op_sel_hi:[0,0,0]
	v_mfma_scale_f32_16x16x128_f8f6f4 v[38:41], v[10:17], v[220:227], v[38:41], v189, v190 op_sel_hi:[0,0,0]
	v_mfma_scale_f32_16x16x128_f8f6f4 v[90:93], v[18:25], v[192:199], v[90:93], v189, v190 op_sel_hi:[0,0,0]
	v_mfma_scale_f32_16x16x128_f8f6f4 v[82:85], v[26:33], v[192:199], v[82:85], v189, v190 op_sel_hi:[0,0,0]
	v_mfma_scale_f32_16x16x128_f8f6f4 v[74:77], v[18:25], v[200:207], v[74:77], v189, v190 op_sel_hi:[0,0,0]
	v_mfma_scale_f32_16x16x128_f8f6f4 v[66:69], v[26:33], v[200:207], v[66:69], v189, v190 op_sel_hi:[0,0,0]
	v_mfma_scale_f32_16x16x128_f8f6f4 v[58:61], v[18:25], v[208:215], v[58:61], v189, v190 op_sel_hi:[0,0,0]
	v_mfma_scale_f32_16x16x128_f8f6f4 v[50:53], v[26:33], v[208:215], v[50:53], v189, v190 op_sel_hi:[0,0,0]
	v_mfma_scale_f32_16x16x128_f8f6f4 v[42:45], v[18:25], v[220:227], v[42:45], v189, v190 op_sel_hi:[0,0,0]
	v_mfma_scale_f32_16x16x128_f8f6f4 v[34:37], v[26:33], v[220:227], v[34:37], v189, v190 op_sel_hi:[0,0,0]
	s_barrier
	s_add_i32 s49, s49, 2
	s_add_u32 s4, s4, 0x100
	s_addc_u32 s5, s5, 0
	s_cmp_gt_u32 s49, 13
	v_lshl_add_u64 v[176:177], v[176:177], 0, s[40:41]

.LBB0_1567:
	s_add_u32 s56, s56, 0xb0080
	v_lshl_add_u64 v[176:177], v[2:3], 0, s[44:45]
	s_addc_u32 s57, s57, 0
	s_mov_b32 s53, -2
	ds_read_b128 v[26:29], v186
	ds_read_b128 v[30:33], v186 offset:1024
	ds_read_b128 v[18:21], v186 offset:2048
	ds_read_b128 v[22:25], v186 offset:3072
	ds_read_b128 v[10:13], v187
	ds_read_b128 v[14:17], v187 offset:1024
	ds_read_b128 v[2:5], v187 offset:2048
	ds_read_b128 v[6:9], v187 offset:3072
	s_add_u32 s58, s56, 0xfff50080
	s_addc_u32 s59, s57, -1
	s_cmp_eq_u32 s53, 40
	s_cselect_b64 vcc, -1, 0
	s_cselect_b32 s59, s5, s59
	s_cselect_b32 s58, s4, s58
	v_cndmask_b32_e32 v179, v177, v175, vcc
	v_cndmask_b32_e32 v178, v176, v174, vcc
	v_lshl_add_u64 v[180:181], s[56:57], 0, v[170:171]
	s_add_i32 m0, s61, 0xc000
	ds_read_b128 v[192:195], v188
	ds_read_b128 v[196:199], v188 offset:1024
	ds_read_b128 v[200:203], v188 offset:2048
	ds_read_b128 v[204:207], v188 offset:3072
	ds_read_b128 v[208:211], v188 offset:4096
	ds_read_b128 v[212:215], v188 offset:5120
	ds_read_b128 v[220:223], v188 offset:6144
	ds_read_b128 v[224:227], v188 offset:7168
	global_load_lds_dwordx4 v[180:181], off
	v_lshl_add_u64 v[180:181], s[56:57], 0, v[172:173]
	s_add_i32 m0, s61, 0xe000
	s_nop 0
	global_load_lds_dwordx4 v[180:181], off
	s_waitcnt vmcnt(24)
	s_waitcnt lgkmcnt(0)
	s_barrier
	v_mfma_scale_f32_16x16x128_f8f6f4 v[158:161], v[26:33], v[192:199], 0, v189, v190 op_sel_hi:[0,0,0]
	v_mfma_scale_f32_16x16x128_f8f6f4 v[154:157], v[18:25], v[192:199], 0, v189, v190 op_sel_hi:[0,0,0]
	v_mfma_scale_f32_16x16x128_f8f6f4 v[150:153], v[26:33], v[200:207], 0, v189, v190 op_sel_hi:[0,0,0]
	v_mfma_scale_f32_16x16x128_f8f6f4 v[142:145], v[18:25], v[200:207], 0, v189, v190 op_sel_hi:[0,0,0]
	v_mfma_scale_f32_16x16x128_f8f6f4 v[134:137], v[26:33], v[208:215], 0, v189, v190 op_sel_hi:[0,0,0]
	v_mfma_scale_f32_16x16x128_f8f6f4 v[126:129], v[18:25], v[208:215], 0, v189, v190 op_sel_hi:[0,0,0]
	v_mfma_scale_f32_16x16x128_f8f6f4 v[118:121], v[26:33], v[220:227], 0, v189, v190 op_sel_hi:[0,0,0]
	v_mfma_scale_f32_16x16x128_f8f6f4 v[110:113], v[18:25], v[220:227], 0, v189, v190 op_sel_hi:[0,0,0]
	v_mfma_scale_f32_16x16x128_f8f6f4 v[146:149], v[10:17], v[192:199], 0, v189, v190 op_sel_hi:[0,0,0]
	v_mfma_scale_f32_16x16x128_f8f6f4 v[138:141], v[2:9], v[192:199], 0, v189, v190 op_sel_hi:[0,0,0]
	v_mfma_scale_f32_16x16x128_f8f6f4 v[130:133], v[10:17], v[200:207], 0, v189, v190 op_sel_hi:[0,0,0]
	v_mfma_scale_f32_16x16x128_f8f6f4 v[122:125], v[2:9], v[200:207], 0, v189, v190 op_sel_hi:[0,0,0]
	v_mfma_scale_f32_16x16x128_f8f6f4 v[114:117], v[10:17], v[208:215], 0, v189, v190 op_sel_hi:[0,0,0]
	v_mfma_scale_f32_16x16x128_f8f6f4 v[106:109], v[2:9], v[208:215], 0, v189, v190 op_sel_hi:[0,0,0]
	v_mfma_scale_f32_16x16x128_f8f6f4 v[102:105], v[10:17], v[220:227], 0, v189, v190 op_sel_hi:[0,0,0]
	v_mfma_scale_f32_16x16x128_f8f6f4 v[98:101], v[2:9], v[220:227], 0, v189, v190 op_sel_hi:[0,0,0]
	s_barrier
	s_add_i32 s80, s69, s33
	v_lshl_add_u64 v[178:179], v[178:179], 0, v[164:165]
	s_mov_b32 m0, s80
	ds_read_b128 v[192:195], v188 offset:16384
	ds_read_b128 v[196:199], v188 offset:17408
	ds_read_b128 v[200:203], v188 offset:18432
	ds_read_b128 v[204:207], v188 offset:19456
	ds_read_b128 v[208:211], v188 offset:20480
	ds_read_b128 v[212:215], v188 offset:21504
	ds_read_b128 v[220:223], v188 offset:22528
	ds_read_b128 v[224:227], v188 offset:23552
	global_load_lds_dwordx4 v[178:179], off
	v_lshl_add_u64 v[180:181], v[178:179], 0, s[10:11]
	s_add_i32 m0, s80, 0x2000
	s_add_i32 s80, s70, s33
	global_load_lds_dwordx4 v[180:181], off
	v_lshl_add_u64 v[180:181], v[178:179], 0, s[12:13]
	s_mov_b32 m0, s80
	v_lshl_add_u64 v[182:183], s[58:59], 0, v[168:169]
	global_load_lds_dwordx4 v[180:181], off
	v_lshl_add_u64 v[180:181], v[178:179], 0, s[14:15]
	s_add_i32 m0, s80, 0x2000
	s_nop 0
	global_load_lds_dwordx4 v[180:181], off
	v_lshl_add_u64 v[180:181], s[58:59], 0, v[166:167]
	s_mov_b32 m0, s61
	s_nop 0
	global_load_lds_dwordx4 v[180:181], off
	s_mov_b32 m0, s62
	s_nop 0
	global_load_lds_dwordx4 v[182:183], off
	s_waitcnt vmcnt(24)
	s_waitcnt lgkmcnt(0)
	s_barrier
	v_mfma_scale_f32_16x16x128_f8f6f4 v[94:97], v[26:33], v[192:199], 0, v189, v190 op_sel_hi:[0,0,0]
	v_mfma_scale_f32_16x16x128_f8f6f4 v[90:93], v[18:25], v[192:199], 0, v189, v190 op_sel_hi:[0,0,0]
	v_mfma_scale_f32_16x16x128_f8f6f4 v[86:89], v[26:33], v[200:207], 0, v189, v190 op_sel_hi:[0,0,0]
	v_mfma_scale_f32_16x16x128_f8f6f4 v[78:81], v[18:25], v[200:207], 0, v189, v190 op_sel_hi:[0,0,0]
	v_mfma_scale_f32_16x16x128_f8f6f4 v[70:73], v[26:33], v[208:215], 0, v189, v190 op_sel_hi:[0,0,0]
	v_mfma_scale_f32_16x16x128_f8f6f4 v[62:65], v[18:25], v[208:215], 0, v189, v190 op_sel_hi:[0,0,0]
	v_mfma_scale_f32_16x16x128_f8f6f4 v[54:57], v[26:33], v[220:227], 0, v189, v190 op_sel_hi:[0,0,0]
	v_mfma_scale_f32_16x16x128_f8f6f4 v[46:49], v[18:25], v[220:227], 0, v189, v190 op_sel_hi:[0,0,0]
	v_mfma_scale_f32_16x16x128_f8f6f4 v[82:85], v[10:17], v[192:199], 0, v189, v190 op_sel_hi:[0,0,0]
	v_mfma_scale_f32_16x16x128_f8f6f4 v[74:77], v[2:9], v[192:199], 0, v189, v190 op_sel_hi:[0,0,0]
	v_mfma_scale_f32_16x16x128_f8f6f4 v[66:69], v[10:17], v[200:207], 0, v189, v190 op_sel_hi:[0,0,0]
	v_mfma_scale_f32_16x16x128_f8f6f4 v[58:61], v[2:9], v[200:207], 0, v189, v190 op_sel_hi:[0,0,0]
	v_mfma_scale_f32_16x16x128_f8f6f4 v[50:53], v[10:17], v[208:215], 0, v189, v190 op_sel_hi:[0,0,0]
	v_mfma_scale_f32_16x16x128_f8f6f4 v[42:45], v[2:9], v[208:215], 0, v189, v190 op_sel_hi:[0,0,0]
	v_mfma_scale_f32_16x16x128_f8f6f4 v[38:41], v[10:17], v[220:227], 0, v189, v190 op_sel_hi:[0,0,0]
	v_mfma_scale_f32_16x16x128_f8f6f4 v[34:37], v[2:9], v[220:227], 0, v189, v190 op_sel_hi:[0,0,0]
	s_barrier
	s_add_i32 s80, 0, 0x18000
	s_add_i32 s81, 0, 0x1c000
	v_add_u32_e32 v14, s80, v184
	v_add_u32_e32 v30, s81, v184
	ds_read_b128 v[2:5], v14
	ds_read_b128 v[6:9], v14 offset:1024
	ds_read_b128 v[10:13], v14 offset:2048
	ds_read_b128 v[14:17], v14 offset:3072
	ds_read_b128 v[18:21], v30
	ds_read_b128 v[22:25], v30 offset:1024
	ds_read_b128 v[26:29], v30 offset:2048
	ds_read_b128 v[30:33], v30 offset:3072
	s_add_u32 s58, s58, 0xb0000
	s_addc_u32 s59, s59, 0
	s_mov_b32 m0, s63
	v_lshl_add_u64 v[216:217], s[58:59], 0, v[166:167]
	ds_read_b128 v[192:195], v188 offset:32768
	ds_read_b128 v[196:199], v188 offset:33792
	ds_read_b128 v[200:203], v188 offset:34816
	ds_read_b128 v[204:207], v188 offset:35840
	ds_read_b128 v[208:211], v188 offset:36864
	ds_read_b128 v[212:215], v188 offset:37888
	ds_read_b128 v[220:223], v188 offset:38912
	ds_read_b128 v[224:227], v188 offset:39936
	global_load_lds_dwordx4 v[216:217], off
	v_lshl_add_u64 v[216:217], s[58:59], 0, v[168:169]
	s_mov_b32 m0, s64
	s_nop 0
	global_load_lds_dwordx4 v[216:217], off
	s_waitcnt vmcnt(8)
	s_waitcnt lgkmcnt(0)
	s_barrier
	v_mfma_scale_f32_16x16x128_f8f6f4 v[158:161], v[2:9], v[192:199], v[158:161], v189, v190 op_sel_hi:[0,0,0]
	v_mfma_scale_f32_16x16x128_f8f6f4 v[154:157], v[10:17], v[192:199], v[154:157], v189, v190 op_sel_hi:[0,0,0]
	v_mfma_scale_f32_16x16x128_f8f6f4 v[150:153], v[2:9], v[200:207], v[150:153], v189, v190 op_sel_hi:[0,0,0]
	v_mfma_scale_f32_16x16x128_f8f6f4 v[142:145], v[10:17], v[200:207], v[142:145], v189, v190 op_sel_hi:[0,0,0]
	v_mfma_scale_f32_16x16x128_f8f6f4 v[134:137], v[2:9], v[208:215], v[134:137], v189, v190 op_sel_hi:[0,0,0]
	v_mfma_scale_f32_16x16x128_f8f6f4 v[126:129], v[10:17], v[208:215], v[126:129], v189, v190 op_sel_hi:[0,0,0]
	v_mfma_scale_f32_16x16x128_f8f6f4 v[118:121], v[2:9], v[220:227], v[118:121], v189, v190 op_sel_hi:[0,0,0]
	v_mfma_scale_f32_16x16x128_f8f6f4 v[110:113], v[10:17], v[220:227], v[110:113], v189, v190 op_sel_hi:[0,0,0]
	v_mfma_scale_f32_16x16x128_f8f6f4 v[146:149], v[18:25], v[192:199], v[146:149], v189, v190 op_sel_hi:[0,0,0]
	v_mfma_scale_f32_16x16x128_f8f6f4 v[138:141], v[26:33], v[192:199], v[138:141], v189, v190 op_sel_hi:[0,0,0]
	v_mfma_scale_f32_16x16x128_f8f6f4 v[130:133], v[18:25], v[200:207], v[130:133], v189, v190 op_sel_hi:[0,0,0]
	v_mfma_scale_f32_16x16x128_f8f6f4 v[122:125], v[26:33], v[200:207], v[122:125], v189, v190 op_sel_hi:[0,0,0]
	v_mfma_scale_f32_16x16x128_f8f6f4 v[114:117], v[18:25], v[208:215], v[114:117], v189, v190 op_sel_hi:[0,0,0]
	v_mfma_scale_f32_16x16x128_f8f6f4 v[106:109], v[26:33], v[208:215], v[106:109], v189, v190 op_sel_hi:[0,0,0]
	v_mfma_scale_f32_16x16x128_f8f6f4 v[102:105], v[18:25], v[220:227], v[102:105], v189, v190 op_sel_hi:[0,0,0]
	v_mfma_scale_f32_16x16x128_f8f6f4 v[98:101], v[26:33], v[220:227], v[98:101], v189, v190 op_sel_hi:[0,0,0]
	s_barrier
	s_add_i32 s58, s80, s33
	v_lshl_add_u64 v[216:217], v[178:179], 0, s[24:25]
	s_mov_b32 m0, s58
	ds_read_b128 v[192:195], v188 offset:49152
	ds_read_b128 v[196:199], v188 offset:50176
	ds_read_b128 v[200:203], v188 offset:51200
	ds_read_b128 v[204:207], v188 offset:52224
	ds_read_b128 v[208:211], v188 offset:53248
	ds_read_b128 v[212:215], v188 offset:54272
	ds_read_b128 v[220:223], v188 offset:55296
	ds_read_b128 v[224:227], v188 offset:56320
	global_load_lds_dwordx4 v[216:217], off
	v_lshl_add_u64 v[216:217], v[178:179], 0, s[26:27]
	s_add_i32 m0, s58, 0x2000
	s_add_i32 s58, s81, s33
	global_load_lds_dwordx4 v[216:217], off
	v_lshl_add_u64 v[216:217], v[178:179], 0, s[38:39]
	s_mov_b32 m0, s58
	v_lshl_add_u64 v[178:179], v[178:179], 0, s[40:41]
	global_load_lds_dwordx4 v[216:217], off
	s_add_i32 m0, s58, 0x2000
	s_nop 0
	global_load_lds_dwordx4 v[178:179], off
	v_lshl_add_u64 v[178:179], v[180:181], 0, s[36:37]
	s_mov_b32 m0, s66
	s_nop 0
	global_load_lds_dwordx4 v[178:179], off
	v_lshl_add_u64 v[178:179], v[182:183], 0, s[36:37]
	s_mov_b32 m0, s67
	s_nop 0
	global_load_lds_dwordx4 v[178:179], off
	s_waitcnt vmcnt(8)
	s_waitcnt lgkmcnt(0)
	s_barrier
	v_mfma_scale_f32_16x16x128_f8f6f4 v[94:97], v[2:9], v[192:199], v[94:97], v189, v190 op_sel_hi:[0,0,0]
	v_mfma_scale_f32_16x16x128_f8f6f4 v[90:93], v[10:17], v[192:199], v[90:93], v189, v190 op_sel_hi:[0,0,0]
	v_mfma_scale_f32_16x16x128_f8f6f4 v[86:89], v[2:9], v[200:207], v[86:89], v189, v190 op_sel_hi:[0,0,0]
	v_mfma_scale_f32_16x16x128_f8f6f4 v[78:81], v[10:17], v[200:207], v[78:81], v189, v190 op_sel_hi:[0,0,0]
	v_mfma_scale_f32_16x16x128_f8f6f4 v[70:73], v[2:9], v[208:215], v[70:73], v189, v190 op_sel_hi:[0,0,0]
	v_mfma_scale_f32_16x16x128_f8f6f4 v[62:65], v[10:17], v[208:215], v[62:65], v189, v190 op_sel_hi:[0,0,0]
	v_mfma_scale_f32_16x16x128_f8f6f4 v[54:57], v[2:9], v[220:227], v[54:57], v189, v190 op_sel_hi:[0,0,0]
	v_mfma_scale_f32_16x16x128_f8f6f4 v[46:49], v[10:17], v[220:227], v[46:49], v189, v190 op_sel_hi:[0,0,0]
	v_mfma_scale_f32_16x16x128_f8f6f4 v[82:85], v[18:25], v[192:199], v[82:85], v189, v190 op_sel_hi:[0,0,0]
	v_mfma_scale_f32_16x16x128_f8f6f4 v[74:77], v[26:33], v[192:199], v[74:77], v189, v190 op_sel_hi:[0,0,0]
	v_mfma_scale_f32_16x16x128_f8f6f4 v[66:69], v[18:25], v[200:207], v[66:69], v189, v190 op_sel_hi:[0,0,0]
	v_mfma_scale_f32_16x16x128_f8f6f4 v[58:61], v[26:33], v[200:207], v[58:61], v189, v190 op_sel_hi:[0,0,0]
	v_mfma_scale_f32_16x16x128_f8f6f4 v[50:53], v[18:25], v[208:215], v[50:53], v189, v190 op_sel_hi:[0,0,0]
	v_mfma_scale_f32_16x16x128_f8f6f4 v[42:45], v[26:33], v[208:215], v[42:45], v189, v190 op_sel_hi:[0,0,0]
	v_mfma_scale_f32_16x16x128_f8f6f4 v[38:41], v[18:25], v[220:227], v[38:41], v189, v190 op_sel_hi:[0,0,0]
	v_mfma_scale_f32_16x16x128_f8f6f4 v[34:37], v[26:33], v[220:227], v[34:37], v189, v190 op_sel_hi:[0,0,0]
	s_barrier
	s_add_i32 s53, s53, 2
	s_add_u32 s56, s56, 0x100
	s_addc_u32 s57, s57, 0
	s_cmp_gt_u32 s53, 41
	v_lshl_add_u64 v[176:177], v[176:177], 0, s[44:45]
